# MFMAs of each accumulator (k=0,1) issued back to back in all five GEMM steady loops (accumulate chain, SrcC forwarding)
# speedup vs baseline: 1.0088x; 1.0030x over previous
; #define PG8_MMA(ai, bj, At, Bt) do { __builtin_amdgcn_s_setprio(1); _Pragma("unroll") for (int m = 0; m < 4; ++m) _Pragma("unroll") for (int n = 0; n < 2; ++n) _Pragma("unroll") for (int k = 0; k < 2; ++k) \
;         acc[ai][bj][m][n] = __builtin_amdgcn_mfma_f32_16x16x32_bf16(Bt[n][k], At[m][k], acc[ai][bj][m][n], 0, 0, 0); __builtin_amdgcn_s_setprio(0); } while (0)
; #define PG8_WAIT_V(n) asm volatile("s_waitcnt vmcnt(" #n ")" ::: "memory")
; #define PG8_TRIP_HEAD(T) const int t = (T); const bool last = (t == nt - 2); \
;             const char* a1 = cA + (size_t)(t + 1) * kstep; \
;             const char* a2 = last ? nA : cA + (size_t)(t + 2) * kstep; const char* b2 = last ? nB : cB + (size_t)(t + 2) * kstep; \
;             const char* a3 = a2 + kstep; const char* b3 = b2 + kstep; \
;             if (last && has_next) S.a_ready(nxt);
; template <class Epi, class Sched, bool ALIGN_EPI = false, bool SP2 = false>
; __device__ __forceinline__ void gemm_phase(PG8_LAS unsigned char* lds, const Gemm g, const Sched& S, const Epi& E) {
;     ...
;         if constexpr (SP2) {
;             { PG8_TRIP_HEAD(0) PG8_TRIP_SP2(asm volatile("s_waitcnt vmcnt(%0)" :: "n"(8 + Epi::NST) : "memory"), PG8_MMAZ) }
;             for (int tt = 2; tt < nt; tt += 2) { PG8_TRIP_HEAD(tt) PG8_TRIP_SP2(PG8_WAIT_V(8), PG8_MMA) }
.LBB0_130:
	ds_read_b128 v[144:147], v140
	ds_read_b128 v[148:151], v140 offset:1024
	ds_read_b128 v[152:155], v140 offset:2048
	ds_read_b128 v[156:159], v140 offset:3072
	ds_read_b128 v[164:167], v141
	ds_read_b128 v[168:171], v141 offset:1024
	ds_read_b128 v[172:175], v141 offset:2048
	ds_read_b128 v[176:179], v141 offset:3072
	s_add_u32 s31, s10, 0xfff7c080
	s_addc_u32 s53, s11, -1
	s_cmp_eq_u32 s30, 28
	s_cselect_b32 s55, s25, s53
	s_cselect_b32 s54, s24, s31
	s_cselect_b32 s57, s4, s29
	s_cselect_b32 s56, s5, s28
	s_mov_b32 m0, s23
	v_lshl_add_u64 v[184:185], s[10:11], 0, v[138:139]
	ds_read_b128 v[180:183], v163
	ds_read_b128 v[190:193], v163 offset:1024
	ds_read_b128 v[194:197], v163 offset:2048
	ds_read_b128 v[198:201], v163 offset:3072
	ds_read_b128 v[202:205], v163 offset:4096
	ds_read_b128 v[206:209], v163 offset:5120
	ds_read_b128 v[216:219], v163 offset:6144
	ds_read_b128 v[220:223], v163 offset:7168
	global_load_lds_dwordx4 v[184:185], off
	v_lshl_add_u64 v[184:185], v[184:185], 0, s[96:97]
	s_mov_b32 m0, s33
	s_nop 0
	global_load_lds_dwordx4 v[184:185], off
	s_waitcnt vmcnt(8)
	s_waitcnt lgkmcnt(0)
	s_barrier
	s_setprio 1
	s_waitcnt lgkmcnt(0)
	v_mfma_f32_16x16x32_bf16 v[120:123], v[144:147], v[180:183], v[120:123]
	v_mfma_f32_16x16x32_bf16 v[120:123], v[148:151], v[190:193], v[120:123]
	v_mfma_f32_16x16x32_bf16 v[116:119], v[152:155], v[180:183], v[116:119]
	v_mfma_f32_16x16x32_bf16 v[116:119], v[156:159], v[190:193], v[116:119]
	v_mfma_f32_16x16x32_bf16 v[104:107], v[144:147], v[194:197], v[104:107]
	v_mfma_f32_16x16x32_bf16 v[104:107], v[148:151], v[198:201], v[104:107]
	v_mfma_f32_16x16x32_bf16 v[100:103], v[152:155], v[194:197], v[100:103]
	v_mfma_f32_16x16x32_bf16 v[100:103], v[156:159], v[198:201], v[100:103]
	v_mfma_f32_16x16x32_bf16 v[88:91], v[144:147], v[202:205], v[88:91]
	v_mfma_f32_16x16x32_bf16 v[88:91], v[148:151], v[206:209], v[88:91]
	v_mfma_f32_16x16x32_bf16 v[84:87], v[152:155], v[202:205], v[84:87]
	v_mfma_f32_16x16x32_bf16 v[84:87], v[156:159], v[206:209], v[84:87]
	v_mfma_f32_16x16x32_bf16 v[72:75], v[144:147], v[216:219], v[72:75]
	v_mfma_f32_16x16x32_bf16 v[72:75], v[148:151], v[220:223], v[72:75]
	v_mfma_f32_16x16x32_bf16 v[68:71], v[152:155], v[216:219], v[68:71]
	v_mfma_f32_16x16x32_bf16 v[68:71], v[156:159], v[220:223], v[68:71]
	s_setprio 0
	s_setprio 1
	v_mfma_f32_16x16x32_bf16 v[128:131], v[164:167], v[180:183], v[128:131]
	v_mfma_f32_16x16x32_bf16 v[128:131], v[168:171], v[190:193], v[128:131]
	v_mfma_f32_16x16x32_bf16 v[124:127], v[172:175], v[180:183], v[124:127]
	v_mfma_f32_16x16x32_bf16 v[124:127], v[176:179], v[190:193], v[124:127]
	v_mfma_f32_16x16x32_bf16 v[112:115], v[164:167], v[194:197], v[112:115]
	v_mfma_f32_16x16x32_bf16 v[112:115], v[168:171], v[198:201], v[112:115]
	v_mfma_f32_16x16x32_bf16 v[108:111], v[172:175], v[194:197], v[108:111]
	v_mfma_f32_16x16x32_bf16 v[108:111], v[176:179], v[198:201], v[108:111]
	v_mfma_f32_16x16x32_bf16 v[96:99], v[164:167], v[202:205], v[96:99]
	v_mfma_f32_16x16x32_bf16 v[96:99], v[168:171], v[206:209], v[96:99]
	v_mfma_f32_16x16x32_bf16 v[92:95], v[172:175], v[202:205], v[92:95]
	v_mfma_f32_16x16x32_bf16 v[92:95], v[176:179], v[206:209], v[92:95]
	v_mfma_f32_16x16x32_bf16 v[80:83], v[164:167], v[216:219], v[80:83]
	v_mfma_f32_16x16x32_bf16 v[80:83], v[168:171], v[220:223], v[80:83]
	v_mfma_f32_16x16x32_bf16 v[76:79], v[172:175], v[216:219], v[76:79]
	v_mfma_f32_16x16x32_bf16 v[76:79], v[176:179], v[220:223], v[76:79]
	s_setprio 0
	s_barrier
	s_mov_b32 m0, s45
	v_lshl_add_u64 v[184:185], s[56:57], 0, v[132:133]
	ds_read_b128 v[180:183], v163 offset:16384
	ds_read_b128 v[190:193], v163 offset:17408
	ds_read_b128 v[194:197], v163 offset:18432
	ds_read_b128 v[198:201], v163 offset:19456
	ds_read_b128 v[202:205], v163 offset:20480
	ds_read_b128 v[206:209], v163 offset:21504
	ds_read_b128 v[216:219], v163 offset:22528
	ds_read_b128 v[220:223], v163 offset:23552
	global_load_lds_dwordx4 v[184:185], off
	v_lshl_add_u64 v[186:187], v[184:185], 0, s[90:91]
	s_mov_b32 m0, s46
	s_nop 0
	global_load_lds_dwordx4 v[186:187], off
	v_lshl_add_u64 v[186:187], v[184:185], 0, s[60:61]
	s_mov_b32 m0, s47
	s_nop 0
	global_load_lds_dwordx4 v[186:187], off
	v_lshl_add_u64 v[186:187], v[184:185], 0, s[64:65]
	s_mov_b32 m0, s48
	s_nop 0
	global_load_lds_dwordx4 v[186:187], off
	v_lshl_add_u64 v[186:187], s[54:55], 0, v[134:135]
	s_mov_b32 m0, s37
	v_lshl_add_u64 v[188:189], v[186:187], 0, s[96:97]
	global_load_lds_dwordx4 v[186:187], off
	s_mov_b32 m0, s38
	s_nop 0
	global_load_lds_dwordx4 v[188:189], off
	s_waitcnt vmcnt(8)
	s_waitcnt lgkmcnt(0)
	s_barrier
; #define PG8_MMA(ai, bj, At, Bt) do { __builtin_amdgcn_s_setprio(1); _Pragma("unroll") for (int m = 0; m < 4; ++m) _Pragma("unroll") for (int n = 0; n < 2; ++n) _Pragma("unroll") for (int k = 0; k < 2; ++k) \
;         acc[ai][bj][m][n] = __builtin_amdgcn_mfma_f32_16x16x32_bf16(Bt[n][k], At[m][k], acc[ai][bj][m][n], 0, 0, 0); __builtin_amdgcn_s_setprio(0); } while (0)
; #define PG8_WAIT_V(n) asm volatile("s_waitcnt vmcnt(" #n ")" ::: "memory")
; #define PG8_TRIP_HEAD(T) const int t = (T); const bool last = (t == nt - 2); \
;             const char* a1 = cA + (size_t)(t + 1) * kstep; \
;             const char* a2 = last ? nA : cA + (size_t)(t + 2) * kstep; const char* b2 = last ? nB : cB + (size_t)(t + 2) * kstep; \
;             const char* a3 = a2 + kstep; const char* b3 = b2 + kstep; \
;             if (last && has_next) S.a_ready(nxt);
; template <class Epi, class Sched, bool ALIGN_EPI = false, bool SP2 = false>
; __device__ __forceinline__ void gemm_phase(PG8_LAS unsigned char* lds, const Gemm g, const Sched& S, const Epi& E) {
;     ...
;         if constexpr (SP2) {
;             { PG8_TRIP_HEAD(0) PG8_TRIP_SP2(asm volatile("s_waitcnt vmcnt(%0)" :: "n"(8 + Epi::NST) : "memory"), PG8_MMAZ) }
;             for (int tt = 2; tt < nt; tt += 2) { PG8_TRIP_HEAD(tt) PG8_TRIP_SP2(PG8_WAIT_V(8), PG8_MMA) }
	s_setprio 1
	s_waitcnt lgkmcnt(0)
	v_mfma_f32_16x16x32_bf16 v[56:59], v[144:147], v[180:183], v[56:59]
	v_mfma_f32_16x16x32_bf16 v[56:59], v[148:151], v[190:193], v[56:59]
	v_mfma_f32_16x16x32_bf16 v[52:55], v[152:155], v[180:183], v[52:55]
	v_mfma_f32_16x16x32_bf16 v[52:55], v[156:159], v[190:193], v[52:55]
	v_mfma_f32_16x16x32_bf16 v[40:43], v[144:147], v[194:197], v[40:43]
	v_mfma_f32_16x16x32_bf16 v[40:43], v[148:151], v[198:201], v[40:43]
	v_mfma_f32_16x16x32_bf16 v[36:39], v[152:155], v[194:197], v[36:39]
	v_mfma_f32_16x16x32_bf16 v[36:39], v[156:159], v[198:201], v[36:39]
	v_mfma_f32_16x16x32_bf16 v[24:27], v[144:147], v[202:205], v[24:27]
	v_mfma_f32_16x16x32_bf16 v[24:27], v[148:151], v[206:209], v[24:27]
	v_mfma_f32_16x16x32_bf16 v[20:23], v[152:155], v[202:205], v[20:23]
	v_mfma_f32_16x16x32_bf16 v[20:23], v[156:159], v[206:209], v[20:23]
	v_mfma_f32_16x16x32_bf16 v[8:11], v[144:147], v[216:219], v[8:11]
	v_mfma_f32_16x16x32_bf16 v[8:11], v[148:151], v[220:223], v[8:11]
	v_mfma_f32_16x16x32_bf16 v[4:7], v[152:155], v[216:219], v[4:7]
	v_mfma_f32_16x16x32_bf16 v[4:7], v[156:159], v[220:223], v[4:7]
	s_setprio 0
	s_setprio 1
	v_mfma_f32_16x16x32_bf16 v[64:67], v[164:167], v[180:183], v[64:67]
	v_mfma_f32_16x16x32_bf16 v[64:67], v[168:171], v[190:193], v[64:67]
	v_mfma_f32_16x16x32_bf16 v[60:63], v[172:175], v[180:183], v[60:63]
	v_mfma_f32_16x16x32_bf16 v[60:63], v[176:179], v[190:193], v[60:63]
	v_mfma_f32_16x16x32_bf16 v[48:51], v[164:167], v[194:197], v[48:51]
	v_mfma_f32_16x16x32_bf16 v[48:51], v[168:171], v[198:201], v[48:51]
	v_mfma_f32_16x16x32_bf16 v[44:47], v[172:175], v[194:197], v[44:47]
	v_mfma_f32_16x16x32_bf16 v[44:47], v[176:179], v[198:201], v[44:47]
	v_mfma_f32_16x16x32_bf16 v[32:35], v[164:167], v[202:205], v[32:35]
	v_mfma_f32_16x16x32_bf16 v[32:35], v[168:171], v[206:209], v[32:35]
	v_mfma_f32_16x16x32_bf16 v[28:31], v[172:175], v[202:205], v[28:31]
	v_mfma_f32_16x16x32_bf16 v[28:31], v[176:179], v[206:209], v[28:31]
	v_mfma_f32_16x16x32_bf16 v[16:19], v[164:167], v[216:219], v[16:19]
	v_mfma_f32_16x16x32_bf16 v[16:19], v[168:171], v[220:223], v[16:19]
	v_mfma_f32_16x16x32_bf16 v[12:15], v[172:175], v[216:219], v[12:15]
	v_mfma_f32_16x16x32_bf16 v[12:15], v[176:179], v[220:223], v[12:15]
	s_setprio 0
	s_barrier
	ds_read_b128 v[144:147], v142
	ds_read_b128 v[148:151], v142 offset:1024
	ds_read_b128 v[152:155], v142 offset:2048
	ds_read_b128 v[156:159], v142 offset:3072
	ds_read_b128 v[164:167], v143
	ds_read_b128 v[168:171], v143 offset:1024
	ds_read_b128 v[172:175], v143 offset:2048
	ds_read_b128 v[176:179], v143 offset:3072
	s_mov_b32 m0, s39
	v_lshl_add_u64 v[188:189], v[186:187], 0, s[82:83]
	ds_read_b128 v[180:183], v163 offset:32768
	ds_read_b128 v[190:193], v163 offset:33792
	ds_read_b128 v[194:197], v163 offset:34816
	ds_read_b128 v[198:201], v163 offset:35840
	ds_read_b128 v[202:205], v163 offset:36864
	ds_read_b128 v[206:209], v163 offset:37888
	ds_read_b128 v[216:219], v163 offset:38912
	ds_read_b128 v[220:223], v163 offset:39936
	global_load_lds_dwordx4 v[188:189], off
	v_lshl_add_u64 v[188:189], v[186:187], 0, s[68:69]
	s_mov_b32 m0, s40
	s_nop 0
	global_load_lds_dwordx4 v[188:189], off
	s_waitcnt vmcnt(8)
	s_waitcnt lgkmcnt(0)
	s_barrier
	s_setprio 1
	s_waitcnt lgkmcnt(0)
	v_mfma_f32_16x16x32_bf16 v[120:123], v[144:147], v[180:183], v[120:123]
	v_mfma_f32_16x16x32_bf16 v[120:123], v[148:151], v[190:193], v[120:123]
	v_mfma_f32_16x16x32_bf16 v[116:119], v[152:155], v[180:183], v[116:119]
	v_mfma_f32_16x16x32_bf16 v[116:119], v[156:159], v[190:193], v[116:119]
	v_mfma_f32_16x16x32_bf16 v[104:107], v[144:147], v[194:197], v[104:107]
	v_mfma_f32_16x16x32_bf16 v[104:107], v[148:151], v[198:201], v[104:107]
	v_mfma_f32_16x16x32_bf16 v[100:103], v[152:155], v[194:197], v[100:103]
	v_mfma_f32_16x16x32_bf16 v[100:103], v[156:159], v[198:201], v[100:103]
	v_mfma_f32_16x16x32_bf16 v[88:91], v[144:147], v[202:205], v[88:91]
	v_mfma_f32_16x16x32_bf16 v[88:91], v[148:151], v[206:209], v[88:91]
	v_mfma_f32_16x16x32_bf16 v[84:87], v[152:155], v[202:205], v[84:87]
	v_mfma_f32_16x16x32_bf16 v[84:87], v[156:159], v[206:209], v[84:87]
	v_mfma_f32_16x16x32_bf16 v[72:75], v[144:147], v[216:219], v[72:75]
	v_mfma_f32_16x16x32_bf16 v[72:75], v[148:151], v[220:223], v[72:75]
	v_mfma_f32_16x16x32_bf16 v[68:71], v[152:155], v[216:219], v[68:71]
	v_mfma_f32_16x16x32_bf16 v[68:71], v[156:159], v[220:223], v[68:71]
	s_setprio 0
	s_setprio 1
	v_mfma_f32_16x16x32_bf16 v[128:131], v[164:167], v[180:183], v[128:131]
	v_mfma_f32_16x16x32_bf16 v[128:131], v[168:171], v[190:193], v[128:131]
	v_mfma_f32_16x16x32_bf16 v[124:127], v[172:175], v[180:183], v[124:127]
	v_mfma_f32_16x16x32_bf16 v[124:127], v[176:179], v[190:193], v[124:127]
	v_mfma_f32_16x16x32_bf16 v[112:115], v[164:167], v[194:197], v[112:115]
	v_mfma_f32_16x16x32_bf16 v[112:115], v[168:171], v[198:201], v[112:115]
	v_mfma_f32_16x16x32_bf16 v[108:111], v[172:175], v[194:197], v[108:111]
	v_mfma_f32_16x16x32_bf16 v[108:111], v[176:179], v[198:201], v[108:111]
	v_mfma_f32_16x16x32_bf16 v[96:99], v[164:167], v[202:205], v[96:99]
	v_mfma_f32_16x16x32_bf16 v[96:99], v[168:171], v[206:209], v[96:99]
	v_mfma_f32_16x16x32_bf16 v[92:95], v[172:175], v[202:205], v[92:95]
	v_mfma_f32_16x16x32_bf16 v[92:95], v[176:179], v[206:209], v[92:95]
	v_mfma_f32_16x16x32_bf16 v[80:83], v[164:167], v[216:219], v[80:83]
	v_mfma_f32_16x16x32_bf16 v[80:83], v[168:171], v[220:223], v[80:83]
	v_mfma_f32_16x16x32_bf16 v[76:79], v[172:175], v[216:219], v[76:79]
	v_mfma_f32_16x16x32_bf16 v[76:79], v[176:179], v[220:223], v[76:79]
	s_setprio 0
	s_barrier
; #define PG8_MMA(ai, bj, At, Bt) do { __builtin_amdgcn_s_setprio(1); _Pragma("unroll") for (int m = 0; m < 4; ++m) _Pragma("unroll") for (int n = 0; n < 2; ++n) _Pragma("unroll") for (int k = 0; k < 2; ++k) \
;         acc[ai][bj][m][n] = __builtin_amdgcn_mfma_f32_16x16x32_bf16(Bt[n][k], At[m][k], acc[ai][bj][m][n], 0, 0, 0); __builtin_amdgcn_s_setprio(0); } while (0)
; #define PG8_WAIT_V(n) asm volatile("s_waitcnt vmcnt(" #n ")" ::: "memory")
; #define PG8_BAR __builtin_amdgcn_s_barrier()
; #define PG8_TRIP_HEAD(T) const int t = (T); const bool last = (t == nt - 2); \
;             const char* a1 = cA + (size_t)(t + 1) * kstep; \
;             const char* a2 = last ? nA : cA + (size_t)(t + 2) * kstep; const char* b2 = last ? nB : cB + (size_t)(t + 2) * kstep; \
;             const char* a3 = a2 + kstep; const char* b3 = b2 + kstep; \
;             if (last && has_next) S.a_ready(nxt);
; template <class Epi, class Sched, bool ALIGN_EPI = false, bool SP2 = false>
; __device__ __forceinline__ void gemm_phase(PG8_LAS unsigned char* lds, const Gemm g, const Sched& S, const Epi& E) {
;     ...
;         if constexpr (SP2) {
;             { PG8_TRIP_HEAD(0) PG8_TRIP_SP2(asm volatile("s_waitcnt vmcnt(%0)" :: "n"(8 + Epi::NST) : "memory"), PG8_MMAZ) }
;             for (int tt = 2; tt < nt; tt += 2) { PG8_TRIP_HEAD(tt) PG8_TRIP_SP2(PG8_WAIT_V(8), PG8_MMA) }
;     ...
;         if constexpr (ALIGN_EPI) { if (wr == 0) PG8_BAR; }
	s_mov_b32 m0, s49
	v_lshl_add_u64 v[188:189], v[184:185], 0, s[78:79]
	ds_read_b128 v[180:183], v163 offset:49152
	ds_read_b128 v[190:193], v163 offset:50176
	ds_read_b128 v[194:197], v163 offset:51200
	ds_read_b128 v[198:201], v163 offset:52224
	ds_read_b128 v[202:205], v163 offset:53248
	ds_read_b128 v[206:209], v163 offset:54272
	ds_read_b128 v[216:219], v163 offset:55296
	ds_read_b128 v[220:223], v163 offset:56320
	global_load_lds_dwordx4 v[188:189], off
	v_lshl_add_u64 v[188:189], v[184:185], 0, s[84:85]
	s_mov_b32 m0, s50
	s_nop 0
	global_load_lds_dwordx4 v[188:189], off
	v_lshl_add_u64 v[188:189], v[184:185], 0, s[62:63]
	s_mov_b32 m0, s51
	v_lshl_add_u64 v[184:185], v[184:185], 0, s[66:67]
	global_load_lds_dwordx4 v[188:189], off
	s_mov_b32 m0, s52
	s_nop 0
	global_load_lds_dwordx4 v[184:185], off
	v_lshl_add_u64 v[184:185], v[186:187], 0, s[78:79]
	s_mov_b32 m0, s0
	s_nop 0
	global_load_lds_dwordx4 v[184:185], off
	v_lshl_add_u64 v[184:185], v[186:187], 0, s[92:93]
	s_mov_b32 m0, s41
	s_nop 0
	global_load_lds_dwordx4 v[184:185], off
	s_waitcnt vmcnt(8)
	s_waitcnt lgkmcnt(0)
	s_barrier
	s_setprio 1
	s_waitcnt lgkmcnt(0)
	v_mfma_f32_16x16x32_bf16 v[56:59], v[144:147], v[180:183], v[56:59]
	v_mfma_f32_16x16x32_bf16 v[56:59], v[148:151], v[190:193], v[56:59]
	v_mfma_f32_16x16x32_bf16 v[52:55], v[152:155], v[180:183], v[52:55]
	v_mfma_f32_16x16x32_bf16 v[52:55], v[156:159], v[190:193], v[52:55]
	v_mfma_f32_16x16x32_bf16 v[40:43], v[144:147], v[194:197], v[40:43]
	v_mfma_f32_16x16x32_bf16 v[40:43], v[148:151], v[198:201], v[40:43]
	v_mfma_f32_16x16x32_bf16 v[36:39], v[152:155], v[194:197], v[36:39]
	v_mfma_f32_16x16x32_bf16 v[36:39], v[156:159], v[198:201], v[36:39]
	v_mfma_f32_16x16x32_bf16 v[24:27], v[144:147], v[202:205], v[24:27]
	v_mfma_f32_16x16x32_bf16 v[24:27], v[148:151], v[206:209], v[24:27]
	v_mfma_f32_16x16x32_bf16 v[20:23], v[152:155], v[202:205], v[20:23]
	v_mfma_f32_16x16x32_bf16 v[20:23], v[156:159], v[206:209], v[20:23]
	v_mfma_f32_16x16x32_bf16 v[8:11], v[144:147], v[216:219], v[8:11]
	v_mfma_f32_16x16x32_bf16 v[8:11], v[148:151], v[220:223], v[8:11]
	v_mfma_f32_16x16x32_bf16 v[4:7], v[152:155], v[216:219], v[4:7]
	v_mfma_f32_16x16x32_bf16 v[4:7], v[156:159], v[220:223], v[4:7]
	s_setprio 0
	s_setprio 1
	v_mfma_f32_16x16x32_bf16 v[64:67], v[164:167], v[180:183], v[64:67]
	v_mfma_f32_16x16x32_bf16 v[64:67], v[168:171], v[190:193], v[64:67]
	v_mfma_f32_16x16x32_bf16 v[60:63], v[172:175], v[180:183], v[60:63]
	v_mfma_f32_16x16x32_bf16 v[60:63], v[176:179], v[190:193], v[60:63]
	v_mfma_f32_16x16x32_bf16 v[48:51], v[164:167], v[194:197], v[48:51]
	v_mfma_f32_16x16x32_bf16 v[48:51], v[168:171], v[198:201], v[48:51]
	v_mfma_f32_16x16x32_bf16 v[44:47], v[172:175], v[194:197], v[44:47]
	v_mfma_f32_16x16x32_bf16 v[44:47], v[176:179], v[198:201], v[44:47]
	v_mfma_f32_16x16x32_bf16 v[32:35], v[164:167], v[202:205], v[32:35]
	v_mfma_f32_16x16x32_bf16 v[32:35], v[168:171], v[206:209], v[32:35]
	v_mfma_f32_16x16x32_bf16 v[28:31], v[172:175], v[202:205], v[28:31]
	v_mfma_f32_16x16x32_bf16 v[28:31], v[176:179], v[206:209], v[28:31]
	v_mfma_f32_16x16x32_bf16 v[16:19], v[164:167], v[216:219], v[16:19]
	v_mfma_f32_16x16x32_bf16 v[16:19], v[168:171], v[220:223], v[16:19]
	v_mfma_f32_16x16x32_bf16 v[12:15], v[172:175], v[216:219], v[12:15]
	v_mfma_f32_16x16x32_bf16 v[12:15], v[176:179], v[220:223], v[12:15]
	s_setprio 0
	s_barrier
	s_add_i32 s30, s30, 2
	s_add_u32 s10, s10, 0x100
	s_addc_u32 s11, s11, 0
	s_add_u32 s28, s28, 0x100
	s_addc_u32 s29, s29, 0
	s_cmp_gt_u32 s30, 29
	s_cbranch_scc0 .LBB0_130
	s_and_b64 vcc, exec, s[20:21]
	s_cbranch_vccz .LBB0_133
	s_barrier

;     __device__ bool next(int i, Unit& u) const { const int rounds = nwg / G; if (i >= rounds) return false; return StaticOrder::next(rounds - 1 - i, u); }
;     __device__ bool next(int i, Unit& u) const { const int rounds = nwg / G; if (i >= 2 * rounds) return false; const bool ok = StaticOrder::next(i >= rounds ? i - rounds : i, u); u.z = (i >= rounds) ? 1 : 0; return ok; }
; template <class Epi, class Sched, bool ALIGN_EPI = false, bool SP2 = false>
; __device__ __forceinline__ void gemm_phase(PG8_LAS unsigned char* lds, const Gemm g, const Sched& S, const Epi& E) {
;     ...
;         const bool has_next = S.next(ui + 1, nxt);
;         const char* nA = has_next ? (const char*)S.opA(g, nxt) + (size_t)nxt.pm * tstepA : cA; const char* nB = has_next ? (const char*)S.opB(g, nxt) + (size_t)nxt.pn * tstepB : cB;
.LBB0_233:
	ds_read_b128 v[120:123], v116
	ds_read_b128 v[132:135], v116 offset:1024
	ds_read_b128 v[144:147], v116 offset:2048
	ds_read_b128 v[148:151], v116 offset:3072
	ds_read_b128 v[152:155], v117
	ds_read_b128 v[156:159], v117 offset:1024
	ds_read_b128 v[166:169], v117 offset:2048
	ds_read_b128 v[170:173], v117 offset:3072
	s_add_u32 s49, s26, 0xffea0080
	s_addc_u32 s50, s27, -1
	s_cmpk_eq_i32 s48, 0x54
	s_cselect_b32 s51, s21, s50
	s_cselect_b32 s50, s20, s49
	s_cselect_b32 s53, s23, s25
	s_cselect_b32 s52, s22, s24
	s_mov_b32 m0, s0
	v_lshl_add_u64 v[188:189], s[26:27], 0, v[164:165]
	ds_read_b128 v[180:183], v178
	ds_read_b128 v[184:187], v178 offset:1024
	ds_read_b128 v[190:193], v178 offset:2048
	ds_read_b128 v[194:197], v178 offset:3072
	ds_read_b128 v[198:201], v178 offset:4096
	ds_read_b128 v[202:205], v178 offset:5120
	ds_read_b128 v[206:209], v178 offset:6144
	ds_read_b128 v[216:219], v178 offset:7168
	global_load_lds_dwordx4 v[188:189], off
	v_lshl_add_u64 v[188:189], v[188:189], 0, s[86:87]
	s_mov_b32 m0, s4
	s_nop 0
	global_load_lds_dwordx4 v[188:189], off
	s_waitcnt vmcnt(8)
	s_waitcnt lgkmcnt(0)
	s_barrier
	s_setprio 1
	s_waitcnt lgkmcnt(0)
	v_mfma_f32_16x16x32_bf16 v[140:143], v[120:123], v[180:183], v[140:143]
	v_mfma_f32_16x16x32_bf16 v[140:143], v[132:135], v[184:187], v[140:143]
	v_mfma_f32_16x16x32_bf16 v[136:139], v[144:147], v[180:183], v[136:139]
	v_mfma_f32_16x16x32_bf16 v[136:139], v[148:151], v[184:187], v[136:139]
	v_mfma_f32_16x16x32_bf16 v[112:115], v[120:123], v[190:193], v[112:115]
	v_mfma_f32_16x16x32_bf16 v[112:115], v[132:135], v[194:197], v[112:115]
	v_mfma_f32_16x16x32_bf16 v[108:111], v[144:147], v[190:193], v[108:111]
	v_mfma_f32_16x16x32_bf16 v[108:111], v[148:151], v[194:197], v[108:111]
	v_mfma_f32_16x16x32_bf16 v[96:99], v[120:123], v[198:201], v[96:99]
	v_mfma_f32_16x16x32_bf16 v[96:99], v[132:135], v[202:205], v[96:99]
	v_mfma_f32_16x16x32_bf16 v[92:95], v[144:147], v[198:201], v[92:95]
	v_mfma_f32_16x16x32_bf16 v[92:95], v[148:151], v[202:205], v[92:95]
	v_mfma_f32_16x16x32_bf16 v[80:83], v[120:123], v[206:209], v[80:83]
	v_mfma_f32_16x16x32_bf16 v[80:83], v[132:135], v[216:219], v[80:83]
	v_mfma_f32_16x16x32_bf16 v[76:79], v[144:147], v[206:209], v[76:79]
	v_mfma_f32_16x16x32_bf16 v[76:79], v[148:151], v[216:219], v[76:79]
	s_setprio 0
	s_setprio 1
	v_mfma_f32_16x16x32_bf16 v[128:131], v[152:155], v[180:183], v[128:131]
	v_mfma_f32_16x16x32_bf16 v[128:131], v[156:159], v[184:187], v[128:131]
	v_mfma_f32_16x16x32_bf16 v[124:127], v[166:169], v[180:183], v[124:127]
	v_mfma_f32_16x16x32_bf16 v[124:127], v[170:173], v[184:187], v[124:127]
	v_mfma_f32_16x16x32_bf16 v[104:107], v[152:155], v[190:193], v[104:107]
	v_mfma_f32_16x16x32_bf16 v[104:107], v[156:159], v[194:197], v[104:107]
	v_mfma_f32_16x16x32_bf16 v[100:103], v[166:169], v[190:193], v[100:103]
	v_mfma_f32_16x16x32_bf16 v[100:103], v[170:173], v[194:197], v[100:103]
	v_mfma_f32_16x16x32_bf16 v[88:91], v[152:155], v[198:201], v[88:91]
	v_mfma_f32_16x16x32_bf16 v[88:91], v[156:159], v[202:205], v[88:91]
	v_mfma_f32_16x16x32_bf16 v[84:87], v[166:169], v[198:201], v[84:87]
	v_mfma_f32_16x16x32_bf16 v[84:87], v[170:173], v[202:205], v[84:87]
	v_mfma_f32_16x16x32_bf16 v[72:75], v[152:155], v[206:209], v[72:75]
	v_mfma_f32_16x16x32_bf16 v[72:75], v[156:159], v[216:219], v[72:75]
	v_mfma_f32_16x16x32_bf16 v[68:71], v[166:169], v[206:209], v[68:71]
	v_mfma_f32_16x16x32_bf16 v[68:71], v[170:173], v[216:219], v[68:71]
	s_setprio 0
	s_barrier
	s_mov_b32 m0, s5
	v_lshl_add_u64 v[188:189], s[52:53], 0, v[162:163]
	ds_read_b128 v[180:183], v178 offset:16384
	ds_read_b128 v[184:187], v178 offset:17408
	ds_read_b128 v[190:193], v178 offset:18432
	ds_read_b128 v[194:197], v178 offset:19456
	ds_read_b128 v[198:201], v178 offset:20480
	ds_read_b128 v[202:205], v178 offset:21504
	ds_read_b128 v[206:209], v178 offset:22528
	ds_read_b128 v[216:219], v178 offset:23552
	global_load_lds_dwordx4 v[188:189], off
	v_lshl_add_u64 v[214:215], v[188:189], 0, s[86:87]
	s_mov_b32 m0, s33
	s_nop 0
	global_load_lds_dwordx4 v[214:215], off
	v_lshl_add_u64 v[214:215], v[188:189], 0, s[54:55]
	s_mov_b32 m0, s42
	s_nop 0
	global_load_lds_dwordx4 v[214:215], off
	v_lshl_add_u64 v[214:215], v[188:189], 0, s[56:57]
	s_mov_b32 m0, s43
	s_nop 0
	global_load_lds_dwordx4 v[214:215], off
	v_lshl_add_u64 v[214:215], s[50:51], 0, v[160:161]
	s_mov_b32 m0, s31
	v_lshl_add_u64 v[220:221], v[214:215], 0, s[86:87]
	global_load_lds_dwordx4 v[214:215], off
	s_mov_b32 m0, s34
	s_nop 0
	global_load_lds_dwordx4 v[220:221], off
	s_waitcnt vmcnt(8)
	s_waitcnt lgkmcnt(0)
	s_barrier
	s_setprio 1
	s_waitcnt lgkmcnt(0)
	v_mfma_f32_16x16x32_bf16 v[56:59], v[120:123], v[180:183], v[56:59]
	v_mfma_f32_16x16x32_bf16 v[56:59], v[132:135], v[184:187], v[56:59]
	v_mfma_f32_16x16x32_bf16 v[52:55], v[144:147], v[180:183], v[52:55]
	v_mfma_f32_16x16x32_bf16 v[52:55], v[148:151], v[184:187], v[52:55]
	v_mfma_f32_16x16x32_bf16 v[48:51], v[120:123], v[190:193], v[48:51]
	v_mfma_f32_16x16x32_bf16 v[48:51], v[132:135], v[194:197], v[48:51]
	v_mfma_f32_16x16x32_bf16 v[44:47], v[144:147], v[190:193], v[44:47]
	v_mfma_f32_16x16x32_bf16 v[44:47], v[148:151], v[194:197], v[44:47]
	v_mfma_f32_16x16x32_bf16 v[32:35], v[120:123], v[198:201], v[32:35]
	v_mfma_f32_16x16x32_bf16 v[32:35], v[132:135], v[202:205], v[32:35]
	v_mfma_f32_16x16x32_bf16 v[28:31], v[144:147], v[198:201], v[28:31]
	v_mfma_f32_16x16x32_bf16 v[28:31], v[148:151], v[202:205], v[28:31]
	v_mfma_f32_16x16x32_bf16 v[16:19], v[120:123], v[206:209], v[16:19]
	v_mfma_f32_16x16x32_bf16 v[16:19], v[132:135], v[216:219], v[16:19]
	v_mfma_f32_16x16x32_bf16 v[12:15], v[144:147], v[206:209], v[12:15]
	v_mfma_f32_16x16x32_bf16 v[12:15], v[148:151], v[216:219], v[12:15]
	s_setprio 0
	s_setprio 1
	v_mfma_f32_16x16x32_bf16 v[64:67], v[152:155], v[180:183], v[64:67]
	v_mfma_f32_16x16x32_bf16 v[64:67], v[156:159], v[184:187], v[64:67]
	v_mfma_f32_16x16x32_bf16 v[60:63], v[166:169], v[180:183], v[60:63]
	v_mfma_f32_16x16x32_bf16 v[60:63], v[170:173], v[184:187], v[60:63]
	v_mfma_f32_16x16x32_bf16 v[40:43], v[152:155], v[190:193], v[40:43]
	v_mfma_f32_16x16x32_bf16 v[40:43], v[156:159], v[194:197], v[40:43]
	v_mfma_f32_16x16x32_bf16 v[36:39], v[166:169], v[190:193], v[36:39]
	v_mfma_f32_16x16x32_bf16 v[36:39], v[170:173], v[194:197], v[36:39]
	v_mfma_f32_16x16x32_bf16 v[24:27], v[152:155], v[198:201], v[24:27]
	v_mfma_f32_16x16x32_bf16 v[24:27], v[156:159], v[202:205], v[24:27]
	v_mfma_f32_16x16x32_bf16 v[20:23], v[166:169], v[198:201], v[20:23]
	v_mfma_f32_16x16x32_bf16 v[20:23], v[170:173], v[202:205], v[20:23]
	v_mfma_f32_16x16x32_bf16 v[8:11], v[152:155], v[206:209], v[8:11]
	v_mfma_f32_16x16x32_bf16 v[8:11], v[156:159], v[216:219], v[8:11]
	v_mfma_f32_16x16x32_bf16 v[4:7], v[166:169], v[206:209], v[4:7]
	v_mfma_f32_16x16x32_bf16 v[4:7], v[170:173], v[216:219], v[4:7]
	s_setprio 0
	s_barrier
	ds_read_b128 v[120:123], v118
	ds_read_b128 v[132:135], v118 offset:1024
	ds_read_b128 v[144:147], v118 offset:2048
	ds_read_b128 v[148:151], v118 offset:3072
	ds_read_b128 v[152:155], v119
	ds_read_b128 v[156:159], v119 offset:1024
	ds_read_b128 v[166:169], v119 offset:2048
	ds_read_b128 v[170:173], v119 offset:3072
	s_mov_b32 m0, s35
	v_lshl_add_u64 v[220:221], v[214:215], 0, s[54:55]
	ds_read_b128 v[180:183], v178 offset:32768
	ds_read_b128 v[184:187], v178 offset:33792
	ds_read_b128 v[190:193], v178 offset:34816
	ds_read_b128 v[194:197], v178 offset:35840
	ds_read_b128 v[198:201], v178 offset:36864
	ds_read_b128 v[202:205], v178 offset:37888
	ds_read_b128 v[206:209], v178 offset:38912
	ds_read_b128 v[216:219], v178 offset:39936
	global_load_lds_dwordx4 v[220:221], off
	v_lshl_add_u64 v[220:221], v[214:215], 0, s[56:57]
	s_mov_b32 m0, s36
	s_nop 0
	global_load_lds_dwordx4 v[220:221], off
	s_waitcnt vmcnt(8)
	s_waitcnt lgkmcnt(0)
	s_barrier
	s_setprio 1
	s_waitcnt lgkmcnt(0)
	v_mfma_f32_16x16x32_bf16 v[140:143], v[120:123], v[180:183], v[140:143]
	v_mfma_f32_16x16x32_bf16 v[140:143], v[132:135], v[184:187], v[140:143]
	v_mfma_f32_16x16x32_bf16 v[136:139], v[144:147], v[180:183], v[136:139]
	v_mfma_f32_16x16x32_bf16 v[136:139], v[148:151], v[184:187], v[136:139]
	v_mfma_f32_16x16x32_bf16 v[112:115], v[120:123], v[190:193], v[112:115]
	v_mfma_f32_16x16x32_bf16 v[112:115], v[132:135], v[194:197], v[112:115]
	v_mfma_f32_16x16x32_bf16 v[108:111], v[144:147], v[190:193], v[108:111]
	v_mfma_f32_16x16x32_bf16 v[108:111], v[148:151], v[194:197], v[108:111]
	v_mfma_f32_16x16x32_bf16 v[96:99], v[120:123], v[198:201], v[96:99]
	v_mfma_f32_16x16x32_bf16 v[96:99], v[132:135], v[202:205], v[96:99]
	v_mfma_f32_16x16x32_bf16 v[92:95], v[144:147], v[198:201], v[92:95]
	v_mfma_f32_16x16x32_bf16 v[92:95], v[148:151], v[202:205], v[92:95]
	v_mfma_f32_16x16x32_bf16 v[80:83], v[120:123], v[206:209], v[80:83]
	v_mfma_f32_16x16x32_bf16 v[80:83], v[132:135], v[216:219], v[80:83]
	v_mfma_f32_16x16x32_bf16 v[76:79], v[144:147], v[206:209], v[76:79]
	v_mfma_f32_16x16x32_bf16 v[76:79], v[148:151], v[216:219], v[76:79]
	s_setprio 0
	s_setprio 1
	v_mfma_f32_16x16x32_bf16 v[128:131], v[152:155], v[180:183], v[128:131]
	v_mfma_f32_16x16x32_bf16 v[128:131], v[156:159], v[184:187], v[128:131]
	v_mfma_f32_16x16x32_bf16 v[124:127], v[166:169], v[180:183], v[124:127]
	v_mfma_f32_16x16x32_bf16 v[124:127], v[170:173], v[184:187], v[124:127]
	v_mfma_f32_16x16x32_bf16 v[104:107], v[152:155], v[190:193], v[104:107]
	v_mfma_f32_16x16x32_bf16 v[104:107], v[156:159], v[194:197], v[104:107]
	v_mfma_f32_16x16x32_bf16 v[100:103], v[166:169], v[190:193], v[100:103]
	v_mfma_f32_16x16x32_bf16 v[100:103], v[170:173], v[194:197], v[100:103]
	v_mfma_f32_16x16x32_bf16 v[88:91], v[152:155], v[198:201], v[88:91]
	v_mfma_f32_16x16x32_bf16 v[88:91], v[156:159], v[202:205], v[88:91]
	v_mfma_f32_16x16x32_bf16 v[84:87], v[166:169], v[198:201], v[84:87]
	v_mfma_f32_16x16x32_bf16 v[84:87], v[170:173], v[202:205], v[84:87]
	v_mfma_f32_16x16x32_bf16 v[72:75], v[152:155], v[206:209], v[72:75]
	v_mfma_f32_16x16x32_bf16 v[72:75], v[156:159], v[216:219], v[72:75]
	v_mfma_f32_16x16x32_bf16 v[68:71], v[166:169], v[206:209], v[68:71]
	v_mfma_f32_16x16x32_bf16 v[68:71], v[170:173], v[216:219], v[68:71]
	s_setprio 0
	s_barrier
; #define PG8_MMA(ai, bj, At, Bt) do { __builtin_amdgcn_s_setprio(1); _Pragma("unroll") for (int m = 0; m < 4; ++m) _Pragma("unroll") for (int n = 0; n < 2; ++n) _Pragma("unroll") for (int k = 0; k < 2; ++k) \
;         acc[ai][bj][m][n] = __builtin_amdgcn_mfma_f32_16x16x32_bf16(Bt[n][k], At[m][k], acc[ai][bj][m][n], 0, 0, 0); __builtin_amdgcn_s_setprio(0); } while (0)
; #define PG8_WAIT_V(n) asm volatile("s_waitcnt vmcnt(" #n ")" ::: "memory")
; #define PG8_TRIP_HEAD(T) const int t = (T); const bool last = (t == nt - 2); \
;             const char* a1 = cA + (size_t)(t + 1) * kstep; \
;             const char* a2 = last ? nA : cA + (size_t)(t + 2) * kstep; const char* b2 = last ? nB : cB + (size_t)(t + 2) * kstep; \
;             const char* a3 = a2 + kstep; const char* b3 = b2 + kstep; \
;             if (last && has_next) S.a_ready(nxt);
; template <class Epi, class Sched, bool ALIGN_EPI = false, bool SP2 = false>
; __device__ __forceinline__ void gemm_phase(PG8_LAS unsigned char* lds, const Gemm g, const Sched& S, const Epi& E) {
;     ...
;         if constexpr (SP2) {
;             { PG8_TRIP_HEAD(0) PG8_TRIP_SP2(asm volatile("s_waitcnt vmcnt(%0)" :: "n"(8 + Epi::NST) : "memory"), PG8_MMAZ) }
;             for (int tt = 2; tt < nt; tt += 2) { PG8_TRIP_HEAD(tt) PG8_TRIP_SP2(PG8_WAIT_V(8), PG8_MMA) }
	s_mov_b32 m0, s44
	v_lshl_add_u64 v[220:221], v[188:189], 0, s[78:79]
	ds_read_b128 v[180:183], v178 offset:49152
	ds_read_b128 v[184:187], v178 offset:50176
	ds_read_b128 v[190:193], v178 offset:51200
	ds_read_b128 v[194:197], v178 offset:52224
	ds_read_b128 v[198:201], v178 offset:53248
	ds_read_b128 v[202:205], v178 offset:54272
	ds_read_b128 v[206:209], v178 offset:55296
	ds_read_b128 v[216:219], v178 offset:56320
	global_load_lds_dwordx4 v[220:221], off
	v_lshl_add_u64 v[220:221], v[188:189], 0, s[60:61]
	s_mov_b32 m0, s45
	s_nop 0
	global_load_lds_dwordx4 v[220:221], off
	v_lshl_add_u64 v[220:221], v[188:189], 0, s[62:63]
	s_mov_b32 m0, s46
	v_lshl_add_u64 v[188:189], v[188:189], 0, s[64:65]
	global_load_lds_dwordx4 v[220:221], off
	s_mov_b32 m0, s47
	s_nop 0
	global_load_lds_dwordx4 v[188:189], off
	v_lshl_add_u64 v[188:189], v[214:215], 0, s[78:79]
	s_mov_b32 m0, s37
	s_nop 0
	global_load_lds_dwordx4 v[188:189], off
	v_lshl_add_u64 v[188:189], v[214:215], 0, s[60:61]
	s_mov_b32 m0, s38
	s_nop 0
	global_load_lds_dwordx4 v[188:189], off
	s_waitcnt vmcnt(8)
	s_waitcnt lgkmcnt(0)
	s_barrier
	s_setprio 1
	s_waitcnt lgkmcnt(0)
	v_mfma_f32_16x16x32_bf16 v[56:59], v[120:123], v[180:183], v[56:59]
	v_mfma_f32_16x16x32_bf16 v[56:59], v[132:135], v[184:187], v[56:59]
	v_mfma_f32_16x16x32_bf16 v[52:55], v[144:147], v[180:183], v[52:55]
	v_mfma_f32_16x16x32_bf16 v[52:55], v[148:151], v[184:187], v[52:55]
	v_mfma_f32_16x16x32_bf16 v[48:51], v[120:123], v[190:193], v[48:51]
	v_mfma_f32_16x16x32_bf16 v[48:51], v[132:135], v[194:197], v[48:51]
	v_mfma_f32_16x16x32_bf16 v[44:47], v[144:147], v[190:193], v[44:47]
	v_mfma_f32_16x16x32_bf16 v[44:47], v[148:151], v[194:197], v[44:47]
	v_mfma_f32_16x16x32_bf16 v[32:35], v[120:123], v[198:201], v[32:35]
	v_mfma_f32_16x16x32_bf16 v[32:35], v[132:135], v[202:205], v[32:35]
	v_mfma_f32_16x16x32_bf16 v[28:31], v[144:147], v[198:201], v[28:31]
	v_mfma_f32_16x16x32_bf16 v[28:31], v[148:151], v[202:205], v[28:31]
	v_mfma_f32_16x16x32_bf16 v[16:19], v[120:123], v[206:209], v[16:19]
	v_mfma_f32_16x16x32_bf16 v[16:19], v[132:135], v[216:219], v[16:19]
	v_mfma_f32_16x16x32_bf16 v[12:15], v[144:147], v[206:209], v[12:15]
	v_mfma_f32_16x16x32_bf16 v[12:15], v[148:151], v[216:219], v[12:15]
	s_setprio 0
	s_setprio 1
	v_mfma_f32_16x16x32_bf16 v[64:67], v[152:155], v[180:183], v[64:67]
	v_mfma_f32_16x16x32_bf16 v[64:67], v[156:159], v[184:187], v[64:67]
	v_mfma_f32_16x16x32_bf16 v[60:63], v[166:169], v[180:183], v[60:63]
	v_mfma_f32_16x16x32_bf16 v[60:63], v[170:173], v[184:187], v[60:63]
	v_mfma_f32_16x16x32_bf16 v[40:43], v[152:155], v[190:193], v[40:43]
	v_mfma_f32_16x16x32_bf16 v[40:43], v[156:159], v[194:197], v[40:43]
	v_mfma_f32_16x16x32_bf16 v[36:39], v[166:169], v[190:193], v[36:39]
	v_mfma_f32_16x16x32_bf16 v[36:39], v[170:173], v[194:197], v[36:39]
	v_mfma_f32_16x16x32_bf16 v[24:27], v[152:155], v[198:201], v[24:27]
	v_mfma_f32_16x16x32_bf16 v[24:27], v[156:159], v[202:205], v[24:27]
	v_mfma_f32_16x16x32_bf16 v[20:23], v[166:169], v[198:201], v[20:23]
	v_mfma_f32_16x16x32_bf16 v[20:23], v[170:173], v[202:205], v[20:23]
	v_mfma_f32_16x16x32_bf16 v[8:11], v[152:155], v[206:209], v[8:11]
	v_mfma_f32_16x16x32_bf16 v[8:11], v[156:159], v[216:219], v[8:11]
	v_mfma_f32_16x16x32_bf16 v[4:7], v[166:169], v[206:209], v[4:7]
	v_mfma_f32_16x16x32_bf16 v[4:7], v[170:173], v[216:219], v[4:7]
	s_setprio 0
	s_barrier
	s_add_i32 s48, s48, 2
	s_add_u32 s26, s26, 0x100
	s_addc_u32 s27, s27, 0
	s_add_u32 s24, s24, 0x100
	s_addc_u32 s25, s25, 0
	s_cmpk_gt_u32 s48, 0x55
	s_cbranch_scc0 .LBB0_233
	s_and_b64 vcc, exec, s[18:19]
	s_cbranch_vccz .LBB0_236
	s_barrier

;     __device__ bool next(int i, Unit& u) const { const int rounds = nwg / G; if (i >= rounds) return false; return StaticOrder::next(rounds - 1 - i, u); }
;     __device__ bool next(int i, Unit& u) const { const int rounds = nwg / G; if (i >= 2 * rounds) return false; const bool ok = StaticOrder::next(i >= rounds ? i - rounds : i, u); u.z = (i >= rounds) ? 1 : 0; return ok; }
; template <class Epi, class Sched, bool ALIGN_EPI = false, bool SP2 = false>
; __device__ __forceinline__ void gemm_phase(PG8_LAS unsigned char* lds, const Gemm g, const Sched& S, const Epi& E) {
;     ...
;         const bool has_next = S.next(ui + 1, nxt);
;         const char* nA = has_next ? (const char*)S.opA(g, nxt) + (size_t)nxt.pm * tstepA : cA; const char* nB = has_next ? (const char*)S.opB(g, nxt) + (size_t)nxt.pn * tstepB : cB;
.LBB0_324:
	ds_read_b128 v[136:139], v132
	ds_read_b128 v[140:143], v132 offset:1024
	ds_read_b128 v[144:147], v132 offset:2048
	ds_read_b128 v[148:151], v132 offset:3072
	ds_read_b128 v[152:155], v133
	ds_read_b128 v[156:159], v133 offset:1024
	ds_read_b128 v[160:163], v133 offset:2048
	ds_read_b128 v[174:177], v133 offset:3072
	s_add_u32 s15, s10, 0xfff7c080
	s_addc_u32 s50, s11, -1
	s_cmp_eq_u32 s14, 28
	s_cselect_b32 s51, s25, s50
	s_cselect_b32 s50, s24, s15
	s_cselect_b32 s53, s3, s13
	s_cselect_b32 s52, s4, s12
	s_mov_b32 m0, s5
	v_lshl_add_u64 v[194:195], s[10:11], 0, v[172:173]
	ds_read_b128 v[178:181], v200
	ds_read_b128 v[182:185], v200 offset:1024
	ds_read_b128 v[186:189], v200 offset:2048
	ds_read_b128 v[190:193], v200 offset:3072
	ds_read_b128 v[202:205], v200 offset:4096
	ds_read_b128 v[206:209], v200 offset:5120
	ds_read_b128 v[216:219], v200 offset:6144
	ds_read_b128 v[220:223], v200 offset:7168
	global_load_lds_dwordx4 v[194:195], off
	v_lshl_add_u64 v[194:195], v[194:195], 0, s[96:97]
	s_mov_b32 m0, s23
	s_nop 0
	global_load_lds_dwordx4 v[194:195], off
	s_waitcnt vmcnt(8)
	s_waitcnt lgkmcnt(0)
	s_barrier
	s_setprio 1
	s_waitcnt lgkmcnt(0)
	v_mfma_f32_16x16x32_bf16 v[120:123], v[136:139], v[178:181], v[120:123]
	v_mfma_f32_16x16x32_bf16 v[120:123], v[140:143], v[182:185], v[120:123]
	v_mfma_f32_16x16x32_bf16 v[116:119], v[144:147], v[178:181], v[116:119]
	v_mfma_f32_16x16x32_bf16 v[116:119], v[148:151], v[182:185], v[116:119]
	v_mfma_f32_16x16x32_bf16 v[104:107], v[136:139], v[186:189], v[104:107]
	v_mfma_f32_16x16x32_bf16 v[104:107], v[140:143], v[190:193], v[104:107]
	v_mfma_f32_16x16x32_bf16 v[100:103], v[144:147], v[186:189], v[100:103]
	v_mfma_f32_16x16x32_bf16 v[100:103], v[148:151], v[190:193], v[100:103]
	v_mfma_f32_16x16x32_bf16 v[88:91], v[136:139], v[202:205], v[88:91]
	v_mfma_f32_16x16x32_bf16 v[88:91], v[140:143], v[206:209], v[88:91]
	v_mfma_f32_16x16x32_bf16 v[84:87], v[144:147], v[202:205], v[84:87]
	v_mfma_f32_16x16x32_bf16 v[84:87], v[148:151], v[206:209], v[84:87]
	v_mfma_f32_16x16x32_bf16 v[72:75], v[136:139], v[216:219], v[72:75]
	v_mfma_f32_16x16x32_bf16 v[72:75], v[140:143], v[220:223], v[72:75]
	v_mfma_f32_16x16x32_bf16 v[68:71], v[144:147], v[216:219], v[68:71]
	v_mfma_f32_16x16x32_bf16 v[68:71], v[148:151], v[220:223], v[68:71]
	s_setprio 0
	s_setprio 1
	v_mfma_f32_16x16x32_bf16 v[128:131], v[152:155], v[178:181], v[128:131]
	v_mfma_f32_16x16x32_bf16 v[128:131], v[156:159], v[182:185], v[128:131]
	v_mfma_f32_16x16x32_bf16 v[124:127], v[160:163], v[178:181], v[124:127]
	v_mfma_f32_16x16x32_bf16 v[124:127], v[174:177], v[182:185], v[124:127]
	v_mfma_f32_16x16x32_bf16 v[112:115], v[152:155], v[186:189], v[112:115]
	v_mfma_f32_16x16x32_bf16 v[112:115], v[156:159], v[190:193], v[112:115]
	v_mfma_f32_16x16x32_bf16 v[108:111], v[160:163], v[186:189], v[108:111]
	v_mfma_f32_16x16x32_bf16 v[108:111], v[174:177], v[190:193], v[108:111]
	v_mfma_f32_16x16x32_bf16 v[96:99], v[152:155], v[202:205], v[96:99]
	v_mfma_f32_16x16x32_bf16 v[96:99], v[156:159], v[206:209], v[96:99]
	v_mfma_f32_16x16x32_bf16 v[92:95], v[160:163], v[202:205], v[92:95]
	v_mfma_f32_16x16x32_bf16 v[92:95], v[174:177], v[206:209], v[92:95]
	v_mfma_f32_16x16x32_bf16 v[80:83], v[152:155], v[216:219], v[80:83]
	v_mfma_f32_16x16x32_bf16 v[80:83], v[156:159], v[220:223], v[80:83]
	v_mfma_f32_16x16x32_bf16 v[76:79], v[160:163], v[216:219], v[76:79]
	v_mfma_f32_16x16x32_bf16 v[76:79], v[174:177], v[220:223], v[76:79]
	s_setprio 0
	s_barrier
	s_mov_b32 m0, s28
	v_lshl_add_u64 v[194:195], s[52:53], 0, v[164:165]
	ds_read_b128 v[178:181], v200 offset:16384
	ds_read_b128 v[182:185], v200 offset:17408
	ds_read_b128 v[186:189], v200 offset:18432
	ds_read_b128 v[190:193], v200 offset:19456
	ds_read_b128 v[202:205], v200 offset:20480
	ds_read_b128 v[206:209], v200 offset:21504
	ds_read_b128 v[216:219], v200 offset:22528
	ds_read_b128 v[220:223], v200 offset:23552
	global_load_lds_dwordx4 v[194:195], off
	v_lshl_add_u64 v[214:215], v[194:195], 0, s[90:91]
	s_mov_b32 m0, s29
	s_nop 0
	global_load_lds_dwordx4 v[214:215], off
	v_lshl_add_u64 v[214:215], v[194:195], 0, s[54:55]
	s_mov_b32 m0, s33
	s_nop 0
	global_load_lds_dwordx4 v[214:215], off
	v_lshl_add_u64 v[214:215], v[194:195], 0, s[60:61]
	s_mov_b32 m0, s45
	s_nop 0
	global_load_lds_dwordx4 v[214:215], off
	v_lshl_add_u64 v[214:215], s[50:51], 0, v[166:167]
	s_mov_b32 m0, s30
	v_lshl_add_u64 v[224:225], v[214:215], 0, s[96:97]
	global_load_lds_dwordx4 v[214:215], off
	s_mov_b32 m0, s31
	s_nop 0
	global_load_lds_dwordx4 v[224:225], off
	s_waitcnt vmcnt(8)
	s_waitcnt lgkmcnt(0)
	s_barrier
	s_setprio 1
	s_waitcnt lgkmcnt(0)
	v_mfma_f32_16x16x32_bf16 v[56:59], v[136:139], v[178:181], v[56:59]
	v_mfma_f32_16x16x32_bf16 v[56:59], v[140:143], v[182:185], v[56:59]
	v_mfma_f32_16x16x32_bf16 v[52:55], v[144:147], v[178:181], v[52:55]
	v_mfma_f32_16x16x32_bf16 v[52:55], v[148:151], v[182:185], v[52:55]
	v_mfma_f32_16x16x32_bf16 v[40:43], v[136:139], v[186:189], v[40:43]
	v_mfma_f32_16x16x32_bf16 v[40:43], v[140:143], v[190:193], v[40:43]
	v_mfma_f32_16x16x32_bf16 v[36:39], v[144:147], v[186:189], v[36:39]
	v_mfma_f32_16x16x32_bf16 v[36:39], v[148:151], v[190:193], v[36:39]
	v_mfma_f32_16x16x32_bf16 v[24:27], v[136:139], v[202:205], v[24:27]
	v_mfma_f32_16x16x32_bf16 v[24:27], v[140:143], v[206:209], v[24:27]
	v_mfma_f32_16x16x32_bf16 v[20:23], v[144:147], v[202:205], v[20:23]
	v_mfma_f32_16x16x32_bf16 v[20:23], v[148:151], v[206:209], v[20:23]
	v_mfma_f32_16x16x32_bf16 v[8:11], v[136:139], v[216:219], v[8:11]
	v_mfma_f32_16x16x32_bf16 v[8:11], v[140:143], v[220:223], v[8:11]
	v_mfma_f32_16x16x32_bf16 v[4:7], v[144:147], v[216:219], v[4:7]
	v_mfma_f32_16x16x32_bf16 v[4:7], v[148:151], v[220:223], v[4:7]
	s_setprio 0
	s_setprio 1
	v_mfma_f32_16x16x32_bf16 v[64:67], v[152:155], v[178:181], v[64:67]
	v_mfma_f32_16x16x32_bf16 v[64:67], v[156:159], v[182:185], v[64:67]
	v_mfma_f32_16x16x32_bf16 v[60:63], v[160:163], v[178:181], v[60:63]
	v_mfma_f32_16x16x32_bf16 v[60:63], v[174:177], v[182:185], v[60:63]
	v_mfma_f32_16x16x32_bf16 v[48:51], v[152:155], v[186:189], v[48:51]
	v_mfma_f32_16x16x32_bf16 v[48:51], v[156:159], v[190:193], v[48:51]
	v_mfma_f32_16x16x32_bf16 v[44:47], v[160:163], v[186:189], v[44:47]
	v_mfma_f32_16x16x32_bf16 v[44:47], v[174:177], v[190:193], v[44:47]
	v_mfma_f32_16x16x32_bf16 v[32:35], v[152:155], v[202:205], v[32:35]
	v_mfma_f32_16x16x32_bf16 v[32:35], v[156:159], v[206:209], v[32:35]
	v_mfma_f32_16x16x32_bf16 v[28:31], v[160:163], v[202:205], v[28:31]
	v_mfma_f32_16x16x32_bf16 v[28:31], v[174:177], v[206:209], v[28:31]
	v_mfma_f32_16x16x32_bf16 v[16:19], v[152:155], v[216:219], v[16:19]
	v_mfma_f32_16x16x32_bf16 v[16:19], v[156:159], v[220:223], v[16:19]
	v_mfma_f32_16x16x32_bf16 v[12:15], v[160:163], v[216:219], v[12:15]
	v_mfma_f32_16x16x32_bf16 v[12:15], v[174:177], v[220:223], v[12:15]
	s_setprio 0
	s_barrier
	ds_read_b128 v[136:139], v134
	ds_read_b128 v[140:143], v134 offset:1024
	ds_read_b128 v[144:147], v134 offset:2048
	ds_read_b128 v[148:151], v134 offset:3072
	ds_read_b128 v[152:155], v135
	ds_read_b128 v[156:159], v135 offset:1024
	ds_read_b128 v[160:163], v135 offset:2048
	ds_read_b128 v[174:177], v135 offset:3072
	s_mov_b32 m0, s34
	v_lshl_add_u64 v[224:225], v[214:215], 0, s[82:83]
	ds_read_b128 v[178:181], v200 offset:32768
	ds_read_b128 v[182:185], v200 offset:33792
	ds_read_b128 v[186:189], v200 offset:34816
	ds_read_b128 v[190:193], v200 offset:35840
	ds_read_b128 v[202:205], v200 offset:36864
	ds_read_b128 v[206:209], v200 offset:37888
	ds_read_b128 v[216:219], v200 offset:38912
	ds_read_b128 v[220:223], v200 offset:39936
	global_load_lds_dwordx4 v[224:225], off
	v_lshl_add_u64 v[224:225], v[214:215], 0, s[64:65]
	s_mov_b32 m0, s35
	s_nop 0
	global_load_lds_dwordx4 v[224:225], off
	s_waitcnt vmcnt(8)
	s_waitcnt lgkmcnt(0)
	s_barrier
	s_setprio 1
	s_waitcnt lgkmcnt(0)
	v_mfma_f32_16x16x32_bf16 v[120:123], v[136:139], v[178:181], v[120:123]
	v_mfma_f32_16x16x32_bf16 v[120:123], v[140:143], v[182:185], v[120:123]
	v_mfma_f32_16x16x32_bf16 v[116:119], v[144:147], v[178:181], v[116:119]
	v_mfma_f32_16x16x32_bf16 v[116:119], v[148:151], v[182:185], v[116:119]
	v_mfma_f32_16x16x32_bf16 v[104:107], v[136:139], v[186:189], v[104:107]
	v_mfma_f32_16x16x32_bf16 v[104:107], v[140:143], v[190:193], v[104:107]
	v_mfma_f32_16x16x32_bf16 v[100:103], v[144:147], v[186:189], v[100:103]
	v_mfma_f32_16x16x32_bf16 v[100:103], v[148:151], v[190:193], v[100:103]
	v_mfma_f32_16x16x32_bf16 v[88:91], v[136:139], v[202:205], v[88:91]
	v_mfma_f32_16x16x32_bf16 v[88:91], v[140:143], v[206:209], v[88:91]
	v_mfma_f32_16x16x32_bf16 v[84:87], v[144:147], v[202:205], v[84:87]
	v_mfma_f32_16x16x32_bf16 v[84:87], v[148:151], v[206:209], v[84:87]
	v_mfma_f32_16x16x32_bf16 v[72:75], v[136:139], v[216:219], v[72:75]
	v_mfma_f32_16x16x32_bf16 v[72:75], v[140:143], v[220:223], v[72:75]
	v_mfma_f32_16x16x32_bf16 v[68:71], v[144:147], v[216:219], v[68:71]
	v_mfma_f32_16x16x32_bf16 v[68:71], v[148:151], v[220:223], v[68:71]
	s_setprio 0
	s_setprio 1
	v_mfma_f32_16x16x32_bf16 v[128:131], v[152:155], v[178:181], v[128:131]
	v_mfma_f32_16x16x32_bf16 v[128:131], v[156:159], v[182:185], v[128:131]
	v_mfma_f32_16x16x32_bf16 v[124:127], v[160:163], v[178:181], v[124:127]
	v_mfma_f32_16x16x32_bf16 v[124:127], v[174:177], v[182:185], v[124:127]
	v_mfma_f32_16x16x32_bf16 v[112:115], v[152:155], v[186:189], v[112:115]
	v_mfma_f32_16x16x32_bf16 v[112:115], v[156:159], v[190:193], v[112:115]
	v_mfma_f32_16x16x32_bf16 v[108:111], v[160:163], v[186:189], v[108:111]
	v_mfma_f32_16x16x32_bf16 v[108:111], v[174:177], v[190:193], v[108:111]
	v_mfma_f32_16x16x32_bf16 v[96:99], v[152:155], v[202:205], v[96:99]
	v_mfma_f32_16x16x32_bf16 v[96:99], v[156:159], v[206:209], v[96:99]
	v_mfma_f32_16x16x32_bf16 v[92:95], v[160:163], v[202:205], v[92:95]
	v_mfma_f32_16x16x32_bf16 v[92:95], v[174:177], v[206:209], v[92:95]
	v_mfma_f32_16x16x32_bf16 v[80:83], v[152:155], v[216:219], v[80:83]
	v_mfma_f32_16x16x32_bf16 v[80:83], v[156:159], v[220:223], v[80:83]
	v_mfma_f32_16x16x32_bf16 v[76:79], v[160:163], v[216:219], v[76:79]
	v_mfma_f32_16x16x32_bf16 v[76:79], v[174:177], v[220:223], v[76:79]
	s_setprio 0
	s_barrier
; #define PG8_MMA(ai, bj, At, Bt) do { __builtin_amdgcn_s_setprio(1); _Pragma("unroll") for (int m = 0; m < 4; ++m) _Pragma("unroll") for (int n = 0; n < 2; ++n) _Pragma("unroll") for (int k = 0; k < 2; ++k) \
;         acc[ai][bj][m][n] = __builtin_amdgcn_mfma_f32_16x16x32_bf16(Bt[n][k], At[m][k], acc[ai][bj][m][n], 0, 0, 0); __builtin_amdgcn_s_setprio(0); } while (0)
; #define PG8_WAIT_V(n) asm volatile("s_waitcnt vmcnt(" #n ")" ::: "memory")
; #define PG8_TRIP_HEAD(T) const int t = (T); const bool last = (t == nt - 2); \
;             const char* a1 = cA + (size_t)(t + 1) * kstep; \
;             const char* a2 = last ? nA : cA + (size_t)(t + 2) * kstep; const char* b2 = last ? nB : cB + (size_t)(t + 2) * kstep; \
;             const char* a3 = a2 + kstep; const char* b3 = b2 + kstep; \
;             if (last && has_next) S.a_ready(nxt);
; template <class Epi, class Sched, bool ALIGN_EPI = false, bool SP2 = false>
; __device__ __forceinline__ void gemm_phase(PG8_LAS unsigned char* lds, const Gemm g, const Sched& S, const Epi& E) {
;     ...
;         if constexpr (SP2) {
;             { PG8_TRIP_HEAD(0) PG8_TRIP_SP2(asm volatile("s_waitcnt vmcnt(%0)" :: "n"(8 + Epi::NST) : "memory"), PG8_MMAZ) }
;             for (int tt = 2; tt < nt; tt += 2) { PG8_TRIP_HEAD(tt) PG8_TRIP_SP2(PG8_WAIT_V(8), PG8_MMA) }
	s_mov_b32 m0, s46
	v_lshl_add_u64 v[224:225], v[194:195], 0, s[78:79]
	ds_read_b128 v[178:181], v200 offset:49152
	ds_read_b128 v[182:185], v200 offset:50176
	ds_read_b128 v[186:189], v200 offset:51200
	ds_read_b128 v[190:193], v200 offset:52224
	ds_read_b128 v[202:205], v200 offset:53248
	ds_read_b128 v[206:209], v200 offset:54272
	ds_read_b128 v[216:219], v200 offset:55296
	ds_read_b128 v[220:223], v200 offset:56320
	global_load_lds_dwordx4 v[224:225], off
	v_lshl_add_u64 v[224:225], v[194:195], 0, s[84:85]
	s_mov_b32 m0, s47
	s_nop 0
	global_load_lds_dwordx4 v[224:225], off
	v_lshl_add_u64 v[224:225], v[194:195], 0, s[56:57]
	s_mov_b32 m0, s48
	v_lshl_add_u64 v[194:195], v[194:195], 0, s[62:63]
	global_load_lds_dwordx4 v[224:225], off
	s_mov_b32 m0, s49
	s_nop 0
	global_load_lds_dwordx4 v[194:195], off
	v_lshl_add_u64 v[194:195], v[214:215], 0, s[78:79]
	s_mov_b32 m0, s38
	s_nop 0
	global_load_lds_dwordx4 v[194:195], off
	v_lshl_add_u64 v[194:195], v[214:215], 0, s[92:93]
	s_mov_b32 m0, s39
	s_nop 0
	global_load_lds_dwordx4 v[194:195], off
	s_waitcnt vmcnt(8)
	s_waitcnt lgkmcnt(0)
	s_barrier
	s_setprio 1
	s_waitcnt lgkmcnt(0)
	v_mfma_f32_16x16x32_bf16 v[56:59], v[136:139], v[178:181], v[56:59]
	v_mfma_f32_16x16x32_bf16 v[56:59], v[140:143], v[182:185], v[56:59]
	v_mfma_f32_16x16x32_bf16 v[52:55], v[144:147], v[178:181], v[52:55]
	v_mfma_f32_16x16x32_bf16 v[52:55], v[148:151], v[182:185], v[52:55]
	v_mfma_f32_16x16x32_bf16 v[40:43], v[136:139], v[186:189], v[40:43]
	v_mfma_f32_16x16x32_bf16 v[40:43], v[140:143], v[190:193], v[40:43]
	v_mfma_f32_16x16x32_bf16 v[36:39], v[144:147], v[186:189], v[36:39]
	v_mfma_f32_16x16x32_bf16 v[36:39], v[148:151], v[190:193], v[36:39]
	v_mfma_f32_16x16x32_bf16 v[24:27], v[136:139], v[202:205], v[24:27]
	v_mfma_f32_16x16x32_bf16 v[24:27], v[140:143], v[206:209], v[24:27]
	v_mfma_f32_16x16x32_bf16 v[20:23], v[144:147], v[202:205], v[20:23]
	v_mfma_f32_16x16x32_bf16 v[20:23], v[148:151], v[206:209], v[20:23]
	v_mfma_f32_16x16x32_bf16 v[8:11], v[136:139], v[216:219], v[8:11]
	v_mfma_f32_16x16x32_bf16 v[8:11], v[140:143], v[220:223], v[8:11]
	v_mfma_f32_16x16x32_bf16 v[4:7], v[144:147], v[216:219], v[4:7]
	v_mfma_f32_16x16x32_bf16 v[4:7], v[148:151], v[220:223], v[4:7]
	s_setprio 0
	s_setprio 1
	v_mfma_f32_16x16x32_bf16 v[64:67], v[152:155], v[178:181], v[64:67]
	v_mfma_f32_16x16x32_bf16 v[64:67], v[156:159], v[182:185], v[64:67]
	v_mfma_f32_16x16x32_bf16 v[60:63], v[160:163], v[178:181], v[60:63]
	v_mfma_f32_16x16x32_bf16 v[60:63], v[174:177], v[182:185], v[60:63]
	v_mfma_f32_16x16x32_bf16 v[48:51], v[152:155], v[186:189], v[48:51]
	v_mfma_f32_16x16x32_bf16 v[48:51], v[156:159], v[190:193], v[48:51]
	v_mfma_f32_16x16x32_bf16 v[44:47], v[160:163], v[186:189], v[44:47]
	v_mfma_f32_16x16x32_bf16 v[44:47], v[174:177], v[190:193], v[44:47]
	v_mfma_f32_16x16x32_bf16 v[32:35], v[152:155], v[202:205], v[32:35]
	v_mfma_f32_16x16x32_bf16 v[32:35], v[156:159], v[206:209], v[32:35]
	v_mfma_f32_16x16x32_bf16 v[28:31], v[160:163], v[202:205], v[28:31]
	v_mfma_f32_16x16x32_bf16 v[28:31], v[174:177], v[206:209], v[28:31]
	v_mfma_f32_16x16x32_bf16 v[16:19], v[152:155], v[216:219], v[16:19]
	v_mfma_f32_16x16x32_bf16 v[16:19], v[156:159], v[220:223], v[16:19]
	v_mfma_f32_16x16x32_bf16 v[12:15], v[160:163], v[216:219], v[12:15]
	v_mfma_f32_16x16x32_bf16 v[12:15], v[174:177], v[220:223], v[12:15]
	s_setprio 0
	s_barrier
	s_add_i32 s14, s14, 2
	s_add_u32 s10, s10, 0x100
	s_addc_u32 s11, s11, 0
	s_add_u32 s12, s12, 0x100
	s_addc_u32 s13, s13, 0
	s_cmp_gt_u32 s14, 29
	s_cbranch_scc0 .LBB0_324
	s_and_b64 vcc, exec, s[18:19]
	s_cbranch_vccz .LBB0_327
	s_barrier

;     __device__ bool next(int i, Unit& u) const { const int rounds = nwg / G; if (i >= rounds) return false; return StaticOrder::next(rounds - 1 - i, u); }
;     __device__ bool next(int i, Unit& u) const { const int rounds = nwg / G; if (i >= 2 * rounds) return false; const bool ok = StaticOrder::next(i >= rounds ? i - rounds : i, u); u.z = (i >= rounds) ? 1 : 0; return ok; }
; template <class Epi, class Sched, bool ALIGN_EPI = false, bool SP2 = false>
; __device__ __forceinline__ void gemm_phase(PG8_LAS unsigned char* lds, const Gemm g, const Sched& S, const Epi& E) {
;     ...
;         const bool has_next = S.next(ui + 1, nxt);
;         const char* nA = has_next ? (const char*)S.opA(g, nxt) + (size_t)nxt.pm * tstepA : cA; const char* nB = has_next ? (const char*)S.opB(g, nxt) + (size_t)nxt.pn * tstepB : cB;
.LBB0_594:
	ds_read_b128 v[136:139], v116
	ds_read_b128 v[140:143], v116 offset:1024
	ds_read_b128 v[144:147], v116 offset:2048
	ds_read_b128 v[148:151], v116 offset:3072
	ds_read_b128 v[152:155], v117
	ds_read_b128 v[156:159], v117 offset:1024
	ds_read_b128 v[160:163], v117 offset:2048
	ds_read_b128 v[164:167], v117 offset:3072
	s_add_u32 s43, s20, 0xfff7c080
	s_addc_u32 s44, s21, -1
	s_cmp_eq_u32 s15, 28
	s_cselect_b32 s45, s17, s44
	s_cselect_b32 s44, s16, s43
	s_cselect_b32 s47, s4, s9
	s_cselect_b32 s46, s5, s8
	s_mov_b32 m0, s33
	v_lshl_add_u64 v[192:193], s[20:21], 0, v[200:201]
	ds_read_b128 v[168:171], v221
	ds_read_b128 v[172:175], v221 offset:1024
	ds_read_b128 v[176:179], v221 offset:2048
	ds_read_b128 v[180:183], v221 offset:3072
	ds_read_b128 v[184:187], v221 offset:4096
	ds_read_b128 v[188:191], v221 offset:5120
	ds_read_b128 v[202:205], v221 offset:6144
	ds_read_b128 v[206:209], v221 offset:7168
	global_load_lds_dwordx4 v[192:193], off
	v_lshl_add_u64 v[192:193], v[192:193], 0, s[96:97]
	s_mov_b32 m0, s34
	s_nop 0
	global_load_lds_dwordx4 v[192:193], off
	s_waitcnt vmcnt(8)
	s_waitcnt lgkmcnt(0)
	s_barrier
	s_setprio 1
	s_waitcnt lgkmcnt(0)
	v_mfma_f32_16x16x32_bf16 v[130:133], v[136:139], v[168:171], v[130:133]
	v_mfma_f32_16x16x32_bf16 v[130:133], v[140:143], v[172:175], v[130:133]
	v_mfma_f32_16x16x32_bf16 v[126:129], v[144:147], v[168:171], v[126:129]
	v_mfma_f32_16x16x32_bf16 v[126:129], v[148:151], v[172:175], v[126:129]
	v_mfma_f32_16x16x32_bf16 v[112:115], v[136:139], v[176:179], v[112:115]
	v_mfma_f32_16x16x32_bf16 v[112:115], v[140:143], v[180:183], v[112:115]
	v_mfma_f32_16x16x32_bf16 v[108:111], v[144:147], v[176:179], v[108:111]
	v_mfma_f32_16x16x32_bf16 v[108:111], v[148:151], v[180:183], v[108:111]
	v_mfma_f32_16x16x32_bf16 v[96:99], v[136:139], v[184:187], v[96:99]
	v_mfma_f32_16x16x32_bf16 v[96:99], v[140:143], v[188:191], v[96:99]
	v_mfma_f32_16x16x32_bf16 v[92:95], v[144:147], v[184:187], v[92:95]
	v_mfma_f32_16x16x32_bf16 v[92:95], v[148:151], v[188:191], v[92:95]
	v_mfma_f32_16x16x32_bf16 v[80:83], v[136:139], v[202:205], v[80:83]
	v_mfma_f32_16x16x32_bf16 v[80:83], v[140:143], v[206:209], v[80:83]
	v_mfma_f32_16x16x32_bf16 v[76:79], v[144:147], v[202:205], v[76:79]
	v_mfma_f32_16x16x32_bf16 v[76:79], v[148:151], v[206:209], v[76:79]
	s_setprio 0
	s_setprio 1
	v_mfma_f32_16x16x32_bf16 v[122:125], v[152:155], v[168:171], v[122:125]
	v_mfma_f32_16x16x32_bf16 v[122:125], v[156:159], v[172:175], v[122:125]
	v_mfma_f32_16x16x32_bf16 v[118:121], v[160:163], v[168:171], v[118:121]
	v_mfma_f32_16x16x32_bf16 v[118:121], v[164:167], v[172:175], v[118:121]
	v_mfma_f32_16x16x32_bf16 v[104:107], v[152:155], v[176:179], v[104:107]
	v_mfma_f32_16x16x32_bf16 v[104:107], v[156:159], v[180:183], v[104:107]
	v_mfma_f32_16x16x32_bf16 v[100:103], v[160:163], v[176:179], v[100:103]
	v_mfma_f32_16x16x32_bf16 v[100:103], v[164:167], v[180:183], v[100:103]
	v_mfma_f32_16x16x32_bf16 v[88:91], v[152:155], v[184:187], v[88:91]
	v_mfma_f32_16x16x32_bf16 v[88:91], v[156:159], v[188:191], v[88:91]
	v_mfma_f32_16x16x32_bf16 v[84:87], v[160:163], v[184:187], v[84:87]
	v_mfma_f32_16x16x32_bf16 v[84:87], v[164:167], v[188:191], v[84:87]
	v_mfma_f32_16x16x32_bf16 v[72:75], v[152:155], v[202:205], v[72:75]
	v_mfma_f32_16x16x32_bf16 v[72:75], v[156:159], v[206:209], v[72:75]
	v_mfma_f32_16x16x32_bf16 v[68:71], v[160:163], v[202:205], v[68:71]
	v_mfma_f32_16x16x32_bf16 v[68:71], v[164:167], v[206:209], v[68:71]
	s_setprio 0
	s_barrier
	s_mov_b32 m0, s35
	v_lshl_add_u64 v[192:193], s[46:47], 0, v[194:195]
	ds_read_b128 v[168:171], v221 offset:16384
	ds_read_b128 v[172:175], v221 offset:17408
	ds_read_b128 v[176:179], v221 offset:18432
	ds_read_b128 v[180:183], v221 offset:19456
	ds_read_b128 v[184:187], v221 offset:20480
	ds_read_b128 v[188:191], v221 offset:21504
	ds_read_b128 v[202:205], v221 offset:22528
	ds_read_b128 v[206:209], v221 offset:23552
	global_load_lds_dwordx4 v[192:193], off
	v_lshl_add_u64 v[214:215], v[192:193], 0, s[90:91]
	s_mov_b32 m0, s36
	s_nop 0
	global_load_lds_dwordx4 v[214:215], off
	v_lshl_add_u64 v[214:215], v[192:193], 0, s[48:49]
	s_mov_b32 m0, s37
	s_nop 0
	global_load_lds_dwordx4 v[214:215], off
	v_lshl_add_u64 v[214:215], v[192:193], 0, s[52:53]
	s_mov_b32 m0, s38
	s_nop 0
	global_load_lds_dwordx4 v[214:215], off
	v_lshl_add_u64 v[214:215], s[44:45], 0, v[196:197]
	s_mov_b32 m0, s23
	v_lshl_add_u64 v[216:217], v[214:215], 0, s[96:97]
	global_load_lds_dwordx4 v[214:215], off
	s_mov_b32 m0, s24
	s_nop 0
	global_load_lds_dwordx4 v[216:217], off
	s_waitcnt vmcnt(8)
	s_waitcnt lgkmcnt(0)
	s_barrier
	s_setprio 1
	s_waitcnt lgkmcnt(0)
	v_mfma_f32_16x16x32_bf16 v[64:67], v[136:139], v[168:171], v[64:67]
	v_mfma_f32_16x16x32_bf16 v[64:67], v[140:143], v[172:175], v[64:67]
	v_mfma_f32_16x16x32_bf16 v[60:63], v[144:147], v[168:171], v[60:63]
	v_mfma_f32_16x16x32_bf16 v[60:63], v[148:151], v[172:175], v[60:63]
	v_mfma_f32_16x16x32_bf16 v[48:51], v[136:139], v[176:179], v[48:51]
	v_mfma_f32_16x16x32_bf16 v[48:51], v[140:143], v[180:183], v[48:51]
	v_mfma_f32_16x16x32_bf16 v[44:47], v[144:147], v[176:179], v[44:47]
	v_mfma_f32_16x16x32_bf16 v[44:47], v[148:151], v[180:183], v[44:47]
	v_mfma_f32_16x16x32_bf16 v[32:35], v[136:139], v[184:187], v[32:35]
	v_mfma_f32_16x16x32_bf16 v[32:35], v[140:143], v[188:191], v[32:35]
	v_mfma_f32_16x16x32_bf16 v[28:31], v[144:147], v[184:187], v[28:31]
	v_mfma_f32_16x16x32_bf16 v[28:31], v[148:151], v[188:191], v[28:31]
	v_mfma_f32_16x16x32_bf16 v[16:19], v[136:139], v[202:205], v[16:19]
	v_mfma_f32_16x16x32_bf16 v[16:19], v[140:143], v[206:209], v[16:19]
	v_mfma_f32_16x16x32_bf16 v[12:15], v[144:147], v[202:205], v[12:15]
	v_mfma_f32_16x16x32_bf16 v[12:15], v[148:151], v[206:209], v[12:15]
	s_setprio 0
	s_setprio 1
	v_mfma_f32_16x16x32_bf16 v[56:59], v[152:155], v[168:171], v[56:59]
	v_mfma_f32_16x16x32_bf16 v[56:59], v[156:159], v[172:175], v[56:59]
	v_mfma_f32_16x16x32_bf16 v[52:55], v[160:163], v[168:171], v[52:55]
	v_mfma_f32_16x16x32_bf16 v[52:55], v[164:167], v[172:175], v[52:55]
	v_mfma_f32_16x16x32_bf16 v[40:43], v[152:155], v[176:179], v[40:43]
	v_mfma_f32_16x16x32_bf16 v[40:43], v[156:159], v[180:183], v[40:43]
	v_mfma_f32_16x16x32_bf16 v[36:39], v[160:163], v[176:179], v[36:39]
	v_mfma_f32_16x16x32_bf16 v[36:39], v[164:167], v[180:183], v[36:39]
	v_mfma_f32_16x16x32_bf16 v[24:27], v[152:155], v[184:187], v[24:27]
	v_mfma_f32_16x16x32_bf16 v[24:27], v[156:159], v[188:191], v[24:27]
	v_mfma_f32_16x16x32_bf16 v[20:23], v[160:163], v[184:187], v[20:23]
	v_mfma_f32_16x16x32_bf16 v[20:23], v[164:167], v[188:191], v[20:23]
	v_mfma_f32_16x16x32_bf16 v[8:11], v[152:155], v[202:205], v[8:11]
	v_mfma_f32_16x16x32_bf16 v[8:11], v[156:159], v[206:209], v[8:11]
	v_mfma_f32_16x16x32_bf16 v[4:7], v[160:163], v[202:205], v[4:7]
	v_mfma_f32_16x16x32_bf16 v[4:7], v[164:167], v[206:209], v[4:7]
	s_setprio 0
	s_barrier
	ds_read_b128 v[136:139], v134
	ds_read_b128 v[140:143], v134 offset:1024
	ds_read_b128 v[144:147], v134 offset:2048
	ds_read_b128 v[148:151], v134 offset:3072
	ds_read_b128 v[152:155], v135
	ds_read_b128 v[156:159], v135 offset:1024
	ds_read_b128 v[160:163], v135 offset:2048
	ds_read_b128 v[164:167], v135 offset:3072
	s_mov_b32 m0, s25
	v_lshl_add_u64 v[216:217], v[214:215], 0, s[82:83]
	ds_read_b128 v[168:171], v221 offset:32768
	ds_read_b128 v[172:175], v221 offset:33792
	ds_read_b128 v[176:179], v221 offset:34816
	ds_read_b128 v[180:183], v221 offset:35840
	ds_read_b128 v[184:187], v221 offset:36864
	ds_read_b128 v[188:191], v221 offset:37888
	ds_read_b128 v[202:205], v221 offset:38912
	ds_read_b128 v[206:209], v221 offset:39936
	global_load_lds_dwordx4 v[216:217], off
	v_lshl_add_u64 v[216:217], v[214:215], 0, s[56:57]
	s_mov_b32 m0, s26
	s_nop 0
	global_load_lds_dwordx4 v[216:217], off
	s_waitcnt vmcnt(8)
	s_waitcnt lgkmcnt(0)
	s_barrier
	s_setprio 1
	s_waitcnt lgkmcnt(0)
	v_mfma_f32_16x16x32_bf16 v[130:133], v[136:139], v[168:171], v[130:133]
	v_mfma_f32_16x16x32_bf16 v[130:133], v[140:143], v[172:175], v[130:133]
	v_mfma_f32_16x16x32_bf16 v[126:129], v[144:147], v[168:171], v[126:129]
	v_mfma_f32_16x16x32_bf16 v[126:129], v[148:151], v[172:175], v[126:129]
	v_mfma_f32_16x16x32_bf16 v[112:115], v[136:139], v[176:179], v[112:115]
	v_mfma_f32_16x16x32_bf16 v[112:115], v[140:143], v[180:183], v[112:115]
	v_mfma_f32_16x16x32_bf16 v[108:111], v[144:147], v[176:179], v[108:111]
	v_mfma_f32_16x16x32_bf16 v[108:111], v[148:151], v[180:183], v[108:111]
	v_mfma_f32_16x16x32_bf16 v[96:99], v[136:139], v[184:187], v[96:99]
	v_mfma_f32_16x16x32_bf16 v[96:99], v[140:143], v[188:191], v[96:99]
	v_mfma_f32_16x16x32_bf16 v[92:95], v[144:147], v[184:187], v[92:95]
	v_mfma_f32_16x16x32_bf16 v[92:95], v[148:151], v[188:191], v[92:95]
	v_mfma_f32_16x16x32_bf16 v[80:83], v[136:139], v[202:205], v[80:83]
	v_mfma_f32_16x16x32_bf16 v[80:83], v[140:143], v[206:209], v[80:83]
	v_mfma_f32_16x16x32_bf16 v[76:79], v[144:147], v[202:205], v[76:79]
	v_mfma_f32_16x16x32_bf16 v[76:79], v[148:151], v[206:209], v[76:79]
	s_setprio 0
	s_setprio 1
	v_mfma_f32_16x16x32_bf16 v[122:125], v[152:155], v[168:171], v[122:125]
	v_mfma_f32_16x16x32_bf16 v[122:125], v[156:159], v[172:175], v[122:125]
	v_mfma_f32_16x16x32_bf16 v[118:121], v[160:163], v[168:171], v[118:121]
	v_mfma_f32_16x16x32_bf16 v[118:121], v[164:167], v[172:175], v[118:121]
	v_mfma_f32_16x16x32_bf16 v[104:107], v[152:155], v[176:179], v[104:107]
	v_mfma_f32_16x16x32_bf16 v[104:107], v[156:159], v[180:183], v[104:107]
	v_mfma_f32_16x16x32_bf16 v[100:103], v[160:163], v[176:179], v[100:103]
	v_mfma_f32_16x16x32_bf16 v[100:103], v[164:167], v[180:183], v[100:103]
	v_mfma_f32_16x16x32_bf16 v[88:91], v[152:155], v[184:187], v[88:91]
	v_mfma_f32_16x16x32_bf16 v[88:91], v[156:159], v[188:191], v[88:91]
	v_mfma_f32_16x16x32_bf16 v[84:87], v[160:163], v[184:187], v[84:87]
	v_mfma_f32_16x16x32_bf16 v[84:87], v[164:167], v[188:191], v[84:87]
	v_mfma_f32_16x16x32_bf16 v[72:75], v[152:155], v[202:205], v[72:75]
	v_mfma_f32_16x16x32_bf16 v[72:75], v[156:159], v[206:209], v[72:75]
	v_mfma_f32_16x16x32_bf16 v[68:71], v[160:163], v[202:205], v[68:71]
	v_mfma_f32_16x16x32_bf16 v[68:71], v[164:167], v[206:209], v[68:71]
	s_setprio 0
	s_barrier
; #define PG8_MMA(ai, bj, At, Bt) do { __builtin_amdgcn_s_setprio(1); _Pragma("unroll") for (int m = 0; m < 4; ++m) _Pragma("unroll") for (int n = 0; n < 2; ++n) _Pragma("unroll") for (int k = 0; k < 2; ++k) \
;         acc[ai][bj][m][n] = __builtin_amdgcn_mfma_f32_16x16x32_bf16(Bt[n][k], At[m][k], acc[ai][bj][m][n], 0, 0, 0); __builtin_amdgcn_s_setprio(0); } while (0)
; #define PG8_WAIT_V(n) asm volatile("s_waitcnt vmcnt(" #n ")" ::: "memory")
; #define PG8_TRIP_HEAD(T) const int t = (T); const bool last = (t == nt - 2); \
;             const char* a1 = cA + (size_t)(t + 1) * kstep; \
;             const char* a2 = last ? nA : cA + (size_t)(t + 2) * kstep; const char* b2 = last ? nB : cB + (size_t)(t + 2) * kstep; \
;             const char* a3 = a2 + kstep; const char* b3 = b2 + kstep; \
;             if (last && has_next) S.a_ready(nxt);
; template <class Epi, class Sched, bool ALIGN_EPI = false, bool SP2 = false>
; __device__ __forceinline__ void gemm_phase(PG8_LAS unsigned char* lds, const Gemm g, const Sched& S, const Epi& E) {
;     ...
;         if constexpr (SP2) {
;             { PG8_TRIP_HEAD(0) PG8_TRIP_SP2(asm volatile("s_waitcnt vmcnt(%0)" :: "n"(8 + Epi::NST) : "memory"), PG8_MMAZ) }
;             for (int tt = 2; tt < nt; tt += 2) { PG8_TRIP_HEAD(tt) PG8_TRIP_SP2(PG8_WAIT_V(8), PG8_MMA) }
	s_mov_b32 m0, s39
	v_lshl_add_u64 v[216:217], v[192:193], 0, s[78:79]
	ds_read_b128 v[168:171], v221 offset:49152
	ds_read_b128 v[172:175], v221 offset:50176
	ds_read_b128 v[176:179], v221 offset:51200
	ds_read_b128 v[180:183], v221 offset:52224
	ds_read_b128 v[184:187], v221 offset:53248
	ds_read_b128 v[188:191], v221 offset:54272
	ds_read_b128 v[202:205], v221 offset:55296
	ds_read_b128 v[206:209], v221 offset:56320
	global_load_lds_dwordx4 v[216:217], off
	v_lshl_add_u64 v[216:217], v[192:193], 0, s[84:85]
	s_mov_b32 m0, s40
	s_nop 0
	global_load_lds_dwordx4 v[216:217], off
	v_lshl_add_u64 v[216:217], v[192:193], 0, s[50:51]
	s_mov_b32 m0, s41
	v_lshl_add_u64 v[192:193], v[192:193], 0, s[54:55]
	global_load_lds_dwordx4 v[216:217], off
	s_mov_b32 m0, s42
	s_nop 0
	global_load_lds_dwordx4 v[192:193], off
	v_lshl_add_u64 v[192:193], v[214:215], 0, s[78:79]
	s_mov_b32 m0, s27
	s_nop 0
	global_load_lds_dwordx4 v[192:193], off
	v_lshl_add_u64 v[192:193], v[214:215], 0, s[92:93]
	s_mov_b32 m0, s28
	s_nop 0
	global_load_lds_dwordx4 v[192:193], off
	s_waitcnt vmcnt(8)
	s_waitcnt lgkmcnt(0)
	s_barrier
	s_setprio 1
	s_waitcnt lgkmcnt(0)
	v_mfma_f32_16x16x32_bf16 v[64:67], v[136:139], v[168:171], v[64:67]
	v_mfma_f32_16x16x32_bf16 v[64:67], v[140:143], v[172:175], v[64:67]
	v_mfma_f32_16x16x32_bf16 v[60:63], v[144:147], v[168:171], v[60:63]
	v_mfma_f32_16x16x32_bf16 v[60:63], v[148:151], v[172:175], v[60:63]
	v_mfma_f32_16x16x32_bf16 v[48:51], v[136:139], v[176:179], v[48:51]
	v_mfma_f32_16x16x32_bf16 v[48:51], v[140:143], v[180:183], v[48:51]
	v_mfma_f32_16x16x32_bf16 v[44:47], v[144:147], v[176:179], v[44:47]
	v_mfma_f32_16x16x32_bf16 v[44:47], v[148:151], v[180:183], v[44:47]
	v_mfma_f32_16x16x32_bf16 v[32:35], v[136:139], v[184:187], v[32:35]
	v_mfma_f32_16x16x32_bf16 v[32:35], v[140:143], v[188:191], v[32:35]
	v_mfma_f32_16x16x32_bf16 v[28:31], v[144:147], v[184:187], v[28:31]
	v_mfma_f32_16x16x32_bf16 v[28:31], v[148:151], v[188:191], v[28:31]
	v_mfma_f32_16x16x32_bf16 v[16:19], v[136:139], v[202:205], v[16:19]
	v_mfma_f32_16x16x32_bf16 v[16:19], v[140:143], v[206:209], v[16:19]
	v_mfma_f32_16x16x32_bf16 v[12:15], v[144:147], v[202:205], v[12:15]
	v_mfma_f32_16x16x32_bf16 v[12:15], v[148:151], v[206:209], v[12:15]
	s_setprio 0
	s_setprio 1
	v_mfma_f32_16x16x32_bf16 v[56:59], v[152:155], v[168:171], v[56:59]
	v_mfma_f32_16x16x32_bf16 v[56:59], v[156:159], v[172:175], v[56:59]
	v_mfma_f32_16x16x32_bf16 v[52:55], v[160:163], v[168:171], v[52:55]
	v_mfma_f32_16x16x32_bf16 v[52:55], v[164:167], v[172:175], v[52:55]
	v_mfma_f32_16x16x32_bf16 v[40:43], v[152:155], v[176:179], v[40:43]
	v_mfma_f32_16x16x32_bf16 v[40:43], v[156:159], v[180:183], v[40:43]
	v_mfma_f32_16x16x32_bf16 v[36:39], v[160:163], v[176:179], v[36:39]
	v_mfma_f32_16x16x32_bf16 v[36:39], v[164:167], v[180:183], v[36:39]
	v_mfma_f32_16x16x32_bf16 v[24:27], v[152:155], v[184:187], v[24:27]
	v_mfma_f32_16x16x32_bf16 v[24:27], v[156:159], v[188:191], v[24:27]
	v_mfma_f32_16x16x32_bf16 v[20:23], v[160:163], v[184:187], v[20:23]
	v_mfma_f32_16x16x32_bf16 v[20:23], v[164:167], v[188:191], v[20:23]
	v_mfma_f32_16x16x32_bf16 v[8:11], v[152:155], v[202:205], v[8:11]
	v_mfma_f32_16x16x32_bf16 v[8:11], v[156:159], v[206:209], v[8:11]
	v_mfma_f32_16x16x32_bf16 v[4:7], v[160:163], v[202:205], v[4:7]
	v_mfma_f32_16x16x32_bf16 v[4:7], v[164:167], v[206:209], v[4:7]
	s_setprio 0
	s_barrier
	s_add_i32 s15, s15, 2
	s_add_u32 s20, s20, 0x100
	s_addc_u32 s21, s21, 0
	s_add_u32 s8, s8, 0x100
	s_addc_u32 s9, s9, 0
	s_cmp_gt_u32 s15, 29
	s_cbranch_scc0 .LBB0_594
	s_and_b64 vcc, exec, s[12:13]
	s_cbranch_vccz .LBB0_597
	s_barrier

;     __device__ bool next(int i, Unit& u) const { const int rounds = nwg / G; if (i >= rounds) return false; return StaticOrder::next(rounds - 1 - i, u); }
;     __device__ bool next(int i, Unit& u) const { const int rounds = nwg / G; if (i >= 2 * rounds) return false; const bool ok = StaticOrder::next(i >= rounds ? i - rounds : i, u); u.z = (i >= rounds) ? 1 : 0; return ok; }
; template <class Epi, class Sched, bool ALIGN_EPI = false, bool SP2 = false>
; __device__ __forceinline__ void gemm_phase(PG8_LAS unsigned char* lds, const Gemm g, const Sched& S, const Epi& E) {
;     ...
;         const bool has_next = S.next(ui + 1, nxt);
;         const char* nA = has_next ? (const char*)S.opA(g, nxt) + (size_t)nxt.pm * tstepA : cA; const char* nB = has_next ? (const char*)S.opB(g, nxt) + (size_t)nxt.pn * tstepB : cB;
.LBB0_700:
	ds_read_b128 v[120:123], v116
	ds_read_b128 v[132:135], v116 offset:1024
	ds_read_b128 v[144:147], v116 offset:2048
	ds_read_b128 v[148:151], v116 offset:3072
	ds_read_b128 v[152:155], v117
	ds_read_b128 v[156:159], v117 offset:1024
	ds_read_b128 v[166:169], v117 offset:2048
	ds_read_b128 v[170:173], v117 offset:3072
	s_add_u32 s27, s10, 0xfff7c080
	s_addc_u32 s47, s11, -1
	s_cmp_eq_u32 s26, 28
	s_cselect_b32 s49, s21, s47
	s_cselect_b32 s48, s20, s27
	s_cselect_b32 s51, s3, s25
	s_cselect_b32 s50, s4, s24
	s_mov_b32 m0, s5
	v_lshl_add_u64 v[208:209], s[10:11], 0, v[164:165]
	ds_read_b128 v[180:183], v178
	ds_read_b128 v[184:187], v178 offset:1024
	ds_read_b128 v[188:191], v178 offset:2048
	ds_read_b128 v[192:195], v178 offset:3072
	ds_read_b128 v[196:199], v178 offset:4096
	ds_read_b128 v[200:203], v178 offset:5120
	ds_read_b128 v[204:207], v178 offset:6144
	ds_read_b128 v[214:217], v178 offset:7168
	global_load_lds_dwordx4 v[208:209], off
	v_lshl_add_u64 v[208:209], v[208:209], 0, s[96:97]
	s_mov_b32 m0, s19
	s_nop 0
	global_load_lds_dwordx4 v[208:209], off
	s_waitcnt vmcnt(8)
	s_waitcnt lgkmcnt(0)
	s_barrier
	s_setprio 1
	s_waitcnt lgkmcnt(0)
	v_mfma_f32_16x16x32_bf16 v[140:143], v[120:123], v[180:183], v[140:143]
	v_mfma_f32_16x16x32_bf16 v[140:143], v[132:135], v[184:187], v[140:143]
	v_mfma_f32_16x16x32_bf16 v[136:139], v[144:147], v[180:183], v[136:139]
	v_mfma_f32_16x16x32_bf16 v[136:139], v[148:151], v[184:187], v[136:139]
	v_mfma_f32_16x16x32_bf16 v[112:115], v[120:123], v[188:191], v[112:115]
	v_mfma_f32_16x16x32_bf16 v[112:115], v[132:135], v[192:195], v[112:115]
	v_mfma_f32_16x16x32_bf16 v[108:111], v[144:147], v[188:191], v[108:111]
	v_mfma_f32_16x16x32_bf16 v[108:111], v[148:151], v[192:195], v[108:111]
	v_mfma_f32_16x16x32_bf16 v[96:99], v[120:123], v[196:199], v[96:99]
	v_mfma_f32_16x16x32_bf16 v[96:99], v[132:135], v[200:203], v[96:99]
	v_mfma_f32_16x16x32_bf16 v[92:95], v[144:147], v[196:199], v[92:95]
	v_mfma_f32_16x16x32_bf16 v[92:95], v[148:151], v[200:203], v[92:95]
	v_mfma_f32_16x16x32_bf16 v[80:83], v[120:123], v[204:207], v[80:83]
	v_mfma_f32_16x16x32_bf16 v[80:83], v[132:135], v[214:217], v[80:83]
	v_mfma_f32_16x16x32_bf16 v[76:79], v[144:147], v[204:207], v[76:79]
	v_mfma_f32_16x16x32_bf16 v[76:79], v[148:151], v[214:217], v[76:79]
	s_setprio 0
	s_setprio 1
	v_mfma_f32_16x16x32_bf16 v[128:131], v[152:155], v[180:183], v[128:131]
	v_mfma_f32_16x16x32_bf16 v[128:131], v[156:159], v[184:187], v[128:131]
	v_mfma_f32_16x16x32_bf16 v[124:127], v[166:169], v[180:183], v[124:127]
	v_mfma_f32_16x16x32_bf16 v[124:127], v[170:173], v[184:187], v[124:127]
	v_mfma_f32_16x16x32_bf16 v[104:107], v[152:155], v[188:191], v[104:107]
	v_mfma_f32_16x16x32_bf16 v[104:107], v[156:159], v[192:195], v[104:107]
	v_mfma_f32_16x16x32_bf16 v[100:103], v[166:169], v[188:191], v[100:103]
	v_mfma_f32_16x16x32_bf16 v[100:103], v[170:173], v[192:195], v[100:103]
	v_mfma_f32_16x16x32_bf16 v[88:91], v[152:155], v[196:199], v[88:91]
	v_mfma_f32_16x16x32_bf16 v[88:91], v[156:159], v[200:203], v[88:91]
	v_mfma_f32_16x16x32_bf16 v[84:87], v[166:169], v[196:199], v[84:87]
	v_mfma_f32_16x16x32_bf16 v[84:87], v[170:173], v[200:203], v[84:87]
	v_mfma_f32_16x16x32_bf16 v[72:75], v[152:155], v[204:207], v[72:75]
	v_mfma_f32_16x16x32_bf16 v[72:75], v[156:159], v[214:217], v[72:75]
	v_mfma_f32_16x16x32_bf16 v[68:71], v[166:169], v[204:207], v[68:71]
	v_mfma_f32_16x16x32_bf16 v[68:71], v[170:173], v[214:217], v[68:71]
	s_setprio 0
	s_barrier
	s_mov_b32 m0, s33
	v_lshl_add_u64 v[208:209], s[50:51], 0, v[160:161]
	ds_read_b128 v[180:183], v178 offset:16384
	ds_read_b128 v[184:187], v178 offset:17408
	ds_read_b128 v[188:191], v178 offset:18432
	ds_read_b128 v[192:195], v178 offset:19456
	ds_read_b128 v[196:199], v178 offset:20480
	ds_read_b128 v[200:203], v178 offset:21504
	ds_read_b128 v[204:207], v178 offset:22528
	ds_read_b128 v[214:217], v178 offset:23552
	global_load_lds_dwordx4 v[208:209], off
	v_lshl_add_u64 v[218:219], v[208:209], 0, s[90:91]
	s_mov_b32 m0, s40
	s_nop 0
	global_load_lds_dwordx4 v[218:219], off
	v_lshl_add_u64 v[218:219], v[208:209], 0, s[52:53]
	s_mov_b32 m0, s41
	s_nop 0
	global_load_lds_dwordx4 v[218:219], off
	v_lshl_add_u64 v[218:219], v[208:209], 0, s[56:57]
	s_mov_b32 m0, s42
	s_nop 0
	global_load_lds_dwordx4 v[218:219], off
	v_lshl_add_u64 v[218:219], s[48:49], 0, v[162:163]
	s_mov_b32 m0, s29
	v_lshl_add_u64 v[220:221], v[218:219], 0, s[96:97]
	global_load_lds_dwordx4 v[218:219], off
	s_mov_b32 m0, s30
	s_nop 0
	global_load_lds_dwordx4 v[220:221], off
	s_waitcnt vmcnt(8)
	s_waitcnt lgkmcnt(0)
	s_barrier
	s_setprio 1
	s_waitcnt lgkmcnt(0)
	v_mfma_f32_16x16x32_bf16 v[56:59], v[120:123], v[180:183], v[56:59]
	v_mfma_f32_16x16x32_bf16 v[56:59], v[132:135], v[184:187], v[56:59]
	v_mfma_f32_16x16x32_bf16 v[52:55], v[144:147], v[180:183], v[52:55]
	v_mfma_f32_16x16x32_bf16 v[52:55], v[148:151], v[184:187], v[52:55]
	v_mfma_f32_16x16x32_bf16 v[48:51], v[120:123], v[188:191], v[48:51]
	v_mfma_f32_16x16x32_bf16 v[48:51], v[132:135], v[192:195], v[48:51]
	v_mfma_f32_16x16x32_bf16 v[44:47], v[144:147], v[188:191], v[44:47]
	v_mfma_f32_16x16x32_bf16 v[44:47], v[148:151], v[192:195], v[44:47]
	v_mfma_f32_16x16x32_bf16 v[32:35], v[120:123], v[196:199], v[32:35]
	v_mfma_f32_16x16x32_bf16 v[32:35], v[132:135], v[200:203], v[32:35]
	v_mfma_f32_16x16x32_bf16 v[28:31], v[144:147], v[196:199], v[28:31]
	v_mfma_f32_16x16x32_bf16 v[28:31], v[148:151], v[200:203], v[28:31]
	v_mfma_f32_16x16x32_bf16 v[16:19], v[120:123], v[204:207], v[16:19]
	v_mfma_f32_16x16x32_bf16 v[16:19], v[132:135], v[214:217], v[16:19]
	v_mfma_f32_16x16x32_bf16 v[12:15], v[144:147], v[204:207], v[12:15]
	v_mfma_f32_16x16x32_bf16 v[12:15], v[148:151], v[214:217], v[12:15]
	s_setprio 0
	s_setprio 1
	v_mfma_f32_16x16x32_bf16 v[64:67], v[152:155], v[180:183], v[64:67]
	v_mfma_f32_16x16x32_bf16 v[64:67], v[156:159], v[184:187], v[64:67]
	v_mfma_f32_16x16x32_bf16 v[60:63], v[166:169], v[180:183], v[60:63]
	v_mfma_f32_16x16x32_bf16 v[60:63], v[170:173], v[184:187], v[60:63]
	v_mfma_f32_16x16x32_bf16 v[40:43], v[152:155], v[188:191], v[40:43]
	v_mfma_f32_16x16x32_bf16 v[40:43], v[156:159], v[192:195], v[40:43]
	v_mfma_f32_16x16x32_bf16 v[36:39], v[166:169], v[188:191], v[36:39]
	v_mfma_f32_16x16x32_bf16 v[36:39], v[170:173], v[192:195], v[36:39]
	v_mfma_f32_16x16x32_bf16 v[24:27], v[152:155], v[196:199], v[24:27]
	v_mfma_f32_16x16x32_bf16 v[24:27], v[156:159], v[200:203], v[24:27]
	v_mfma_f32_16x16x32_bf16 v[20:23], v[166:169], v[196:199], v[20:23]
	v_mfma_f32_16x16x32_bf16 v[20:23], v[170:173], v[200:203], v[20:23]
	v_mfma_f32_16x16x32_bf16 v[8:11], v[152:155], v[204:207], v[8:11]
	v_mfma_f32_16x16x32_bf16 v[8:11], v[156:159], v[214:217], v[8:11]
	v_mfma_f32_16x16x32_bf16 v[4:7], v[166:169], v[204:207], v[4:7]
	v_mfma_f32_16x16x32_bf16 v[4:7], v[170:173], v[214:217], v[4:7]
	s_setprio 0
	s_barrier
	ds_read_b128 v[120:123], v118
	ds_read_b128 v[132:135], v118 offset:1024
	ds_read_b128 v[144:147], v118 offset:2048
	ds_read_b128 v[148:151], v118 offset:3072
	ds_read_b128 v[152:155], v119
	ds_read_b128 v[156:159], v119 offset:1024
	ds_read_b128 v[166:169], v119 offset:2048
	ds_read_b128 v[170:173], v119 offset:3072
	s_mov_b32 m0, s31
	v_lshl_add_u64 v[220:221], v[218:219], 0, s[82:83]
	ds_read_b128 v[180:183], v178 offset:32768
	ds_read_b128 v[184:187], v178 offset:33792
	ds_read_b128 v[188:191], v178 offset:34816
	ds_read_b128 v[192:195], v178 offset:35840
	ds_read_b128 v[196:199], v178 offset:36864
	ds_read_b128 v[200:203], v178 offset:37888
	ds_read_b128 v[204:207], v178 offset:38912
	ds_read_b128 v[214:217], v178 offset:39936
	global_load_lds_dwordx4 v[220:221], off
	v_lshl_add_u64 v[220:221], v[218:219], 0, s[62:63]
	s_mov_b32 m0, s34
	s_nop 0
	global_load_lds_dwordx4 v[220:221], off
	s_waitcnt vmcnt(8)
	s_waitcnt lgkmcnt(0)
	s_barrier
	s_setprio 1
	s_waitcnt lgkmcnt(0)
	v_mfma_f32_16x16x32_bf16 v[140:143], v[120:123], v[180:183], v[140:143]
	v_mfma_f32_16x16x32_bf16 v[140:143], v[132:135], v[184:187], v[140:143]
	v_mfma_f32_16x16x32_bf16 v[136:139], v[144:147], v[180:183], v[136:139]
	v_mfma_f32_16x16x32_bf16 v[136:139], v[148:151], v[184:187], v[136:139]
	v_mfma_f32_16x16x32_bf16 v[112:115], v[120:123], v[188:191], v[112:115]
	v_mfma_f32_16x16x32_bf16 v[112:115], v[132:135], v[192:195], v[112:115]
	v_mfma_f32_16x16x32_bf16 v[108:111], v[144:147], v[188:191], v[108:111]
	v_mfma_f32_16x16x32_bf16 v[108:111], v[148:151], v[192:195], v[108:111]
	v_mfma_f32_16x16x32_bf16 v[96:99], v[120:123], v[196:199], v[96:99]
	v_mfma_f32_16x16x32_bf16 v[96:99], v[132:135], v[200:203], v[96:99]
	v_mfma_f32_16x16x32_bf16 v[92:95], v[144:147], v[196:199], v[92:95]
	v_mfma_f32_16x16x32_bf16 v[92:95], v[148:151], v[200:203], v[92:95]
	v_mfma_f32_16x16x32_bf16 v[80:83], v[120:123], v[204:207], v[80:83]
	v_mfma_f32_16x16x32_bf16 v[80:83], v[132:135], v[214:217], v[80:83]
	v_mfma_f32_16x16x32_bf16 v[76:79], v[144:147], v[204:207], v[76:79]
	v_mfma_f32_16x16x32_bf16 v[76:79], v[148:151], v[214:217], v[76:79]
	s_setprio 0
	s_setprio 1
	v_mfma_f32_16x16x32_bf16 v[128:131], v[152:155], v[180:183], v[128:131]
	v_mfma_f32_16x16x32_bf16 v[128:131], v[156:159], v[184:187], v[128:131]
	v_mfma_f32_16x16x32_bf16 v[124:127], v[166:169], v[180:183], v[124:127]
	v_mfma_f32_16x16x32_bf16 v[124:127], v[170:173], v[184:187], v[124:127]
	v_mfma_f32_16x16x32_bf16 v[104:107], v[152:155], v[188:191], v[104:107]
	v_mfma_f32_16x16x32_bf16 v[104:107], v[156:159], v[192:195], v[104:107]
	v_mfma_f32_16x16x32_bf16 v[100:103], v[166:169], v[188:191], v[100:103]
	v_mfma_f32_16x16x32_bf16 v[100:103], v[170:173], v[192:195], v[100:103]
	v_mfma_f32_16x16x32_bf16 v[88:91], v[152:155], v[196:199], v[88:91]
	v_mfma_f32_16x16x32_bf16 v[88:91], v[156:159], v[200:203], v[88:91]
	v_mfma_f32_16x16x32_bf16 v[84:87], v[166:169], v[196:199], v[84:87]
	v_mfma_f32_16x16x32_bf16 v[84:87], v[170:173], v[200:203], v[84:87]
	v_mfma_f32_16x16x32_bf16 v[72:75], v[152:155], v[204:207], v[72:75]
	v_mfma_f32_16x16x32_bf16 v[72:75], v[156:159], v[214:217], v[72:75]
	v_mfma_f32_16x16x32_bf16 v[68:71], v[166:169], v[204:207], v[68:71]
	v_mfma_f32_16x16x32_bf16 v[68:71], v[170:173], v[214:217], v[68:71]
	s_setprio 0
	s_barrier
; #define PG8_MMA(ai, bj, At, Bt) do { __builtin_amdgcn_s_setprio(1); _Pragma("unroll") for (int m = 0; m < 4; ++m) _Pragma("unroll") for (int n = 0; n < 2; ++n) _Pragma("unroll") for (int k = 0; k < 2; ++k) \
;         acc[ai][bj][m][n] = __builtin_amdgcn_mfma_f32_16x16x32_bf16(Bt[n][k], At[m][k], acc[ai][bj][m][n], 0, 0, 0); __builtin_amdgcn_s_setprio(0); } while (0)
; #define PG8_WAIT_V(n) asm volatile("s_waitcnt vmcnt(" #n ")" ::: "memory")
; #define PG8_TRIP_HEAD(T) const int t = (T); const bool last = (t == nt - 2); \
;             const char* a1 = cA + (size_t)(t + 1) * kstep; \
;             const char* a2 = last ? nA : cA + (size_t)(t + 2) * kstep; const char* b2 = last ? nB : cB + (size_t)(t + 2) * kstep; \
;             const char* a3 = a2 + kstep; const char* b3 = b2 + kstep; \
;             if (last && has_next) S.a_ready(nxt);
; template <class Epi, class Sched, bool ALIGN_EPI = false, bool SP2 = false>
; __device__ __forceinline__ void gemm_phase(PG8_LAS unsigned char* lds, const Gemm g, const Sched& S, const Epi& E) {
;     ...
;         if constexpr (SP2) {
;             { PG8_TRIP_HEAD(0) PG8_TRIP_SP2(asm volatile("s_waitcnt vmcnt(%0)" :: "n"(8 + Epi::NST) : "memory"), PG8_MMAZ) }
;             for (int tt = 2; tt < nt; tt += 2) { PG8_TRIP_HEAD(tt) PG8_TRIP_SP2(PG8_WAIT_V(8), PG8_MMA) }
	s_mov_b32 m0, s43
	v_lshl_add_u64 v[220:221], v[208:209], 0, s[78:79]
	ds_read_b128 v[180:183], v178 offset:49152
	ds_read_b128 v[184:187], v178 offset:50176
	ds_read_b128 v[188:191], v178 offset:51200
	ds_read_b128 v[192:195], v178 offset:52224
	ds_read_b128 v[196:199], v178 offset:53248
	ds_read_b128 v[200:203], v178 offset:54272
	ds_read_b128 v[204:207], v178 offset:55296
	ds_read_b128 v[214:217], v178 offset:56320
	global_load_lds_dwordx4 v[220:221], off
	v_lshl_add_u64 v[220:221], v[208:209], 0, s[84:85]
	s_mov_b32 m0, s44
	s_nop 0
	global_load_lds_dwordx4 v[220:221], off
	v_lshl_add_u64 v[220:221], v[208:209], 0, s[54:55]
	s_mov_b32 m0, s45
	v_lshl_add_u64 v[208:209], v[208:209], 0, s[60:61]
	global_load_lds_dwordx4 v[220:221], off
	s_mov_b32 m0, s46
	s_nop 0
	global_load_lds_dwordx4 v[208:209], off
	v_lshl_add_u64 v[208:209], v[218:219], 0, s[78:79]
	s_mov_b32 m0, s36
	s_nop 0
	global_load_lds_dwordx4 v[208:209], off
	v_lshl_add_u64 v[208:209], v[218:219], 0, s[92:93]
	s_mov_b32 m0, s37
	s_nop 0
	global_load_lds_dwordx4 v[208:209], off
	s_waitcnt vmcnt(8)
	s_waitcnt lgkmcnt(0)
	s_barrier
	s_setprio 1
	s_waitcnt lgkmcnt(0)
	v_mfma_f32_16x16x32_bf16 v[56:59], v[120:123], v[180:183], v[56:59]
	v_mfma_f32_16x16x32_bf16 v[56:59], v[132:135], v[184:187], v[56:59]
	v_mfma_f32_16x16x32_bf16 v[52:55], v[144:147], v[180:183], v[52:55]
	v_mfma_f32_16x16x32_bf16 v[52:55], v[148:151], v[184:187], v[52:55]
	v_mfma_f32_16x16x32_bf16 v[48:51], v[120:123], v[188:191], v[48:51]
	v_mfma_f32_16x16x32_bf16 v[48:51], v[132:135], v[192:195], v[48:51]
	v_mfma_f32_16x16x32_bf16 v[44:47], v[144:147], v[188:191], v[44:47]
	v_mfma_f32_16x16x32_bf16 v[44:47], v[148:151], v[192:195], v[44:47]
	v_mfma_f32_16x16x32_bf16 v[32:35], v[120:123], v[196:199], v[32:35]
	v_mfma_f32_16x16x32_bf16 v[32:35], v[132:135], v[200:203], v[32:35]
	v_mfma_f32_16x16x32_bf16 v[28:31], v[144:147], v[196:199], v[28:31]
	v_mfma_f32_16x16x32_bf16 v[28:31], v[148:151], v[200:203], v[28:31]
	v_mfma_f32_16x16x32_bf16 v[16:19], v[120:123], v[204:207], v[16:19]
	v_mfma_f32_16x16x32_bf16 v[16:19], v[132:135], v[214:217], v[16:19]
	v_mfma_f32_16x16x32_bf16 v[12:15], v[144:147], v[204:207], v[12:15]
	v_mfma_f32_16x16x32_bf16 v[12:15], v[148:151], v[214:217], v[12:15]
	s_setprio 0
	s_setprio 1
	v_mfma_f32_16x16x32_bf16 v[64:67], v[152:155], v[180:183], v[64:67]
	v_mfma_f32_16x16x32_bf16 v[64:67], v[156:159], v[184:187], v[64:67]
	v_mfma_f32_16x16x32_bf16 v[60:63], v[166:169], v[180:183], v[60:63]
	v_mfma_f32_16x16x32_bf16 v[60:63], v[170:173], v[184:187], v[60:63]
	v_mfma_f32_16x16x32_bf16 v[40:43], v[152:155], v[188:191], v[40:43]
	v_mfma_f32_16x16x32_bf16 v[40:43], v[156:159], v[192:195], v[40:43]
	v_mfma_f32_16x16x32_bf16 v[36:39], v[166:169], v[188:191], v[36:39]
	v_mfma_f32_16x16x32_bf16 v[36:39], v[170:173], v[192:195], v[36:39]
	v_mfma_f32_16x16x32_bf16 v[24:27], v[152:155], v[196:199], v[24:27]
	v_mfma_f32_16x16x32_bf16 v[24:27], v[156:159], v[200:203], v[24:27]
	v_mfma_f32_16x16x32_bf16 v[20:23], v[166:169], v[196:199], v[20:23]
	v_mfma_f32_16x16x32_bf16 v[20:23], v[170:173], v[200:203], v[20:23]
	v_mfma_f32_16x16x32_bf16 v[8:11], v[152:155], v[204:207], v[8:11]
	v_mfma_f32_16x16x32_bf16 v[8:11], v[156:159], v[214:217], v[8:11]
	v_mfma_f32_16x16x32_bf16 v[4:7], v[166:169], v[204:207], v[4:7]
	v_mfma_f32_16x16x32_bf16 v[4:7], v[170:173], v[214:217], v[4:7]
	s_setprio 0
	s_barrier
	s_add_i32 s26, s26, 2
	s_add_u32 s10, s10, 0x100
	s_addc_u32 s11, s11, 0
	s_add_u32 s24, s24, 0x100
	s_addc_u32 s25, s25, 0
	s_cmp_gt_u32 s26, 29
	s_cbranch_scc0 .LBB0_700
	s_and_b64 vcc, exec, s[16:17]
	s_cbranch_vccz .LBB0_703
	s_barrier
